# nt (streaming) hint on the read-once residual/mixer row loads of the LN1+router phase, on top of v40
# speedup vs baseline: 1.0078x; 1.0025x over previous
.LBB0_613:
	s_ashr_i32 s75, s74, 31
	s_lshl_b64 s[0:1], s[74:75], 6
	v_readlane_b32 s4, v238, 14
	s_add_u32 s0, s0, s4
	s_addc_u32 s1, s1, 0
	s_lshl_b64 s[0:1], s[0:1], 10
	v_lshl_add_u64 v[50:51], s[0:1], 0, v[34:35]
	v_lshlrev_b64 v[50:51], 1, v[50:51]
	v_lshl_add_u64 v[52:53], s[76:77], 0, v[50:51]
	s_mov_b64 s[0:1], 0x800
	v_lshl_add_u64 v[54:55], s[92:93], 0, v[50:51]
	global_load_dwordx2 v[76:77], v[52:53], off nt
	global_load_dwordx2 v[92:93], v[52:53], off offset:512 nt
	global_load_dwordx2 v[164:165], v[52:53], off offset:1024 nt
	global_load_dwordx2 v[178:179], v[52:53], off offset:1536 nt
	global_load_dwordx2 v[78:79], v[54:55], off nt
	global_load_dwordx2 v[94:95], v[54:55], off offset:512 nt
	global_load_dwordx2 v[172:173], v[54:55], off offset:1024 nt
	global_load_dwordx2 v[180:181], v[54:55], off offset:1536 nt
	v_lshl_add_u64 v[52:53], v[50:51], 0, s[0:1]
	v_lshl_add_u64 v[54:55], s[76:77], 0, v[52:53]
	v_lshl_add_u64 v[52:53], s[92:93], 0, v[52:53]
	global_load_dwordx2 v[88:89], v[54:55], off nt
	global_load_dwordx2 v[96:97], v[54:55], off offset:512 nt
	global_load_dwordx2 v[174:175], v[54:55], off offset:1024 nt
	global_load_dwordx2 v[184:185], v[54:55], off offset:1536 nt
	global_load_dwordx2 v[90:91], v[52:53], off nt
	global_load_dwordx2 v[98:99], v[52:53], off offset:512 nt
	global_load_dwordx2 v[176:177], v[52:53], off offset:1024 nt
	global_load_dwordx2 v[204:205], v[52:53], off offset:1536 nt
	s_mov_b64 s[0:1], 0x1000
	v_lshl_add_u64 v[52:53], v[50:51], 0, s[0:1]
	v_lshl_add_u64 v[54:55], s[76:77], 0, v[52:53]
	v_lshl_add_u64 v[52:53], s[92:93], 0, v[52:53]
	s_mov_b64 s[0:1], 0x1800
	global_load_dwordx2 v[158:159], v[54:55], off nt
	global_load_dwordx2 v[150:151], v[54:55], off offset:512 nt
	global_load_dwordx2 v[144:145], v[54:55], off offset:1024 nt
	global_load_dwordx2 v[136:137], v[54:55], off offset:1536 nt
	global_load_dwordx2 v[162:163], v[52:53], off nt
	global_load_dwordx2 v[154:155], v[52:53], off offset:512 nt
	global_load_dwordx2 v[146:147], v[52:53], off offset:1024 nt
	global_load_dwordx2 v[138:139], v[52:53], off offset:1536 nt
	v_lshl_add_u64 v[52:53], v[50:51], 0, s[0:1]
	v_lshl_add_u64 v[54:55], s[76:77], 0, v[52:53]
	v_lshl_add_u64 v[52:53], s[92:93], 0, v[52:53]
	global_load_dwordx2 v[156:157], v[54:55], off nt
	global_load_dwordx2 v[148:149], v[54:55], off offset:512 nt
	global_load_dwordx2 v[140:141], v[54:55], off offset:1024 nt
	global_load_dwordx2 v[132:133], v[54:55], off offset:1536 nt
	global_load_dwordx2 v[160:161], v[52:53], off nt
	global_load_dwordx2 v[152:153], v[52:53], off offset:512 nt
	global_load_dwordx2 v[142:143], v[52:53], off offset:1024 nt
	global_load_dwordx2 v[134:135], v[52:53], off offset:1536 nt
	s_mov_b64 s[0:1], 0x2000
	v_lshl_add_u64 v[52:53], v[50:51], 0, s[0:1]
	v_lshl_add_u64 v[54:55], s[76:77], 0, v[52:53]
	v_lshl_add_u64 v[52:53], s[92:93], 0, v[52:53]
	s_mov_b64 s[0:1], 0x2800
	global_load_dwordx2 v[126:127], v[54:55], off nt
	global_load_dwordx2 v[118:119], v[54:55], off offset:512 nt
	global_load_dwordx2 v[112:113], v[54:55], off offset:1024 nt
	global_load_dwordx2 v[104:105], v[54:55], off offset:1536 nt
	global_load_dwordx2 v[130:131], v[52:53], off nt
	global_load_dwordx2 v[122:123], v[52:53], off offset:512 nt
	global_load_dwordx2 v[114:115], v[52:53], off offset:1024 nt
	global_load_dwordx2 v[106:107], v[52:53], off offset:1536 nt
	v_lshl_add_u64 v[52:53], v[50:51], 0, s[0:1]
	v_lshl_add_u64 v[54:55], s[76:77], 0, v[52:53]
	v_lshl_add_u64 v[52:53], s[92:93], 0, v[52:53]
	s_mov_b64 s[0:1], 0x3000
	global_load_dwordx2 v[124:125], v[54:55], off nt
	global_load_dwordx2 v[116:117], v[54:55], off offset:512 nt
	global_load_dwordx2 v[108:109], v[54:55], off offset:1024 nt
	global_load_dwordx2 v[100:101], v[54:55], off offset:1536 nt
	global_load_dwordx2 v[128:129], v[52:53], off nt
	global_load_dwordx2 v[120:121], v[52:53], off offset:512 nt
	global_load_dwordx2 v[110:111], v[52:53], off offset:1024 nt
	global_load_dwordx2 v[102:103], v[52:53], off offset:1536 nt
	v_lshl_add_u64 v[52:53], v[50:51], 0, s[0:1]
	s_mov_b64 s[0:1], 0x3800
	v_readlane_b32 s5, v238, 15
	v_lshl_add_u64 v[54:55], s[76:77], 0, v[52:53]
	v_lshl_add_u64 v[52:53], s[92:93], 0, v[52:53]
	v_lshl_add_u64 v[50:51], v[50:51], 0, s[0:1]
	global_load_dwordx2 v[82:83], v[54:55], off nt
	global_load_dwordx2 v[70:71], v[54:55], off offset:512 nt
	global_load_dwordx2 v[64:65], v[54:55], off offset:1024 nt
	global_load_dwordx2 v[56:57], v[54:55], off offset:1536 nt
	global_load_dwordx2 v[86:87], v[52:53], off nt
	global_load_dwordx2 v[74:75], v[52:53], off offset:512 nt
	global_load_dwordx2 v[66:67], v[52:53], off offset:1024 nt
	global_load_dwordx2 v[58:59], v[52:53], off offset:1536 nt
	v_lshl_add_u64 v[52:53], s[76:77], 0, v[50:51]
	v_lshl_add_u64 v[50:51], s[92:93], 0, v[50:51]
	s_lshl_b64 s[0:1], s[74:75], 17
	global_load_dwordx2 v[80:81], v[52:53], off nt
	global_load_dwordx2 v[68:69], v[52:53], off offset:512 nt
	global_load_dwordx2 v[60:61], v[52:53], off offset:1024 nt
	s_nop 0
	global_load_dwordx2 v[52:53], v[52:53], off offset:1536 nt
	s_nop 0
	global_load_dwordx2 v[84:85], v[50:51], off nt
	global_load_dwordx2 v[72:73], v[50:51], off offset:512 nt
	global_load_dwordx2 v[62:63], v[50:51], off offset:1024 nt
	global_load_dwordx2 v[54:55], v[50:51], off offset:1536 nt
	v_lshl_add_u64 v[50:51], v[36:37], 0, s[0:1]
	s_waitcnt vmcnt(0)
	v_lshlrev_b32_e32 v182, 16, v76
	v_and_b32_e32 v183, 0xffff0000, v76
	v_lshlrev_b32_e32 v76, 16, v77
	v_and_b32_e32 v77, 0xffff0000, v77
	s_waitcnt vmcnt(59)
	v_lshlrev_b32_e32 v206, 16, v78
	v_and_b32_e32 v207, 0xffff0000, v78
	v_lshlrev_b32_e32 v78, 16, v79
	v_and_b32_e32 v79, 0xffff0000, v79
	v_pk_fma_f32 v[76:77], v[76:77], s[96:97], v[78:79] op_sel_hi:[1,0,1]
	v_pk_fma_f32 v[78:79], v[182:183], s[96:97], v[206:207] op_sel_hi:[1,0,1]
	s_waitcnt vmcnt(55)
	v_lshlrev_b32_e32 v182, 16, v88
	v_and_b32_e32 v183, 0xffff0000, v88
	v_lshlrev_b32_e32 v88, 16, v89
	v_and_b32_e32 v89, 0xffff0000, v89
	s_waitcnt vmcnt(51)
	v_lshlrev_b32_e32 v206, 16, v90
	v_and_b32_e32 v207, 0xffff0000, v90
	v_lshlrev_b32_e32 v90, 16, v91
	v_and_b32_e32 v91, 0xffff0000, v91
	v_pk_fma_f32 v[88:89], v[88:89], s[96:97], v[90:91] op_sel_hi:[1,0,1]
	v_pk_fma_f32 v[90:91], v[182:183], s[96:97], v[206:207] op_sel_hi:[1,0,1]
	v_lshlrev_b32_e32 v182, 16, v92
	v_and_b32_e32 v183, 0xffff0000, v92
	v_lshlrev_b32_e32 v92, 16, v93
	v_and_b32_e32 v93, 0xffff0000, v93
	v_lshlrev_b32_e32 v206, 16, v94
	v_and_b32_e32 v207, 0xffff0000, v94
	v_lshlrev_b32_e32 v94, 16, v95
	v_and_b32_e32 v95, 0xffff0000, v95
	v_pk_fma_f32 v[92:93], v[92:93], s[96:97], v[94:95] op_sel_hi:[1,0,1]
	v_pk_fma_f32 v[94:95], v[182:183], s[96:97], v[206:207] op_sel_hi:[1,0,1]
	v_lshlrev_b32_e32 v182, 16, v96
	v_and_b32_e32 v183, 0xffff0000, v96
	v_lshlrev_b32_e32 v96, 16, v97
	v_and_b32_e32 v97, 0xffff0000, v97
	s_waitcnt vmcnt(50)
	v_lshlrev_b32_e32 v206, 16, v98
	v_and_b32_e32 v207, 0xffff0000, v98
	v_lshlrev_b32_e32 v98, 16, v99
	v_and_b32_e32 v99, 0xffff0000, v99
	v_pk_fma_f32 v[96:97], v[96:97], s[96:97], v[98:99] op_sel_hi:[1,0,1]
	v_pk_fma_f32 v[98:99], v[182:183], s[96:97], v[206:207] op_sel_hi:[1,0,1]
	v_lshlrev_b32_e32 v182, 16, v164
	v_and_b32_e32 v183, 0xffff0000, v164
	v_lshlrev_b32_e32 v164, 16, v165
	v_and_b32_e32 v165, 0xffff0000, v165
	v_lshlrev_b32_e32 v206, 16, v172
	v_and_b32_e32 v207, 0xffff0000, v172
	v_lshlrev_b32_e32 v172, 16, v173
	v_and_b32_e32 v173, 0xffff0000, v173
	v_pk_fma_f32 v[164:165], v[164:165], s[96:97], v[172:173] op_sel_hi:[1,0,1]
	v_pk_fma_f32 v[172:173], v[182:183], s[96:97], v[206:207] op_sel_hi:[1,0,1]
	v_lshlrev_b32_e32 v182, 16, v174
	v_and_b32_e32 v183, 0xffff0000, v174
	v_lshlrev_b32_e32 v174, 16, v175
	v_and_b32_e32 v175, 0xffff0000, v175
	s_waitcnt vmcnt(49)
	v_lshlrev_b32_e32 v206, 16, v176
	v_and_b32_e32 v207, 0xffff0000, v176
	v_lshlrev_b32_e32 v176, 16, v177
	v_and_b32_e32 v177, 0xffff0000, v177
	v_pk_fma_f32 v[174:175], v[174:175], s[96:97], v[176:177] op_sel_hi:[1,0,1]
	v_pk_fma_f32 v[176:177], v[182:183], s[96:97], v[206:207] op_sel_hi:[1,0,1]
	v_lshlrev_b32_e32 v182, 16, v178
	v_and_b32_e32 v183, 0xffff0000, v178
	v_lshlrev_b32_e32 v178, 16, v179
	v_and_b32_e32 v179, 0xffff0000, v179
	v_lshlrev_b32_e32 v206, 16, v180
	v_and_b32_e32 v207, 0xffff0000, v180
	v_lshlrev_b32_e32 v180, 16, v181
	v_and_b32_e32 v181, 0xffff0000, v181
	v_pk_fma_f32 v[178:179], v[178:179], s[96:97], v[180:181] op_sel_hi:[1,0,1]
	v_pk_fma_f32 v[182:183], v[182:183], s[96:97], v[206:207] op_sel_hi:[1,0,1]
	v_lshlrev_b32_e32 v206, 16, v184
	v_and_b32_e32 v207, 0xffff0000, v184
	v_lshlrev_b32_e32 v180, 16, v185
	v_and_b32_e32 v181, 0xffff0000, v185
	s_waitcnt vmcnt(48)
	v_lshlrev_b32_e32 v184, 16, v204
	v_and_b32_e32 v185, 0xffff0000, v204
	v_lshlrev_b32_e32 v204, 16, v205
	v_and_b32_e32 v205, 0xffff0000, v205
	v_pk_fma_f32 v[180:181], v[180:181], s[96:97], v[204:205] op_sel_hi:[1,0,1]
	v_pk_fma_f32 v[184:185], v[206:207], s[96:97], v[184:185] op_sel_hi:[1,0,1]
	v_pk_mov_b32 v[204:205], v[78:79], v[76:77] op_sel:[1,0]
	v_mov_b32_e32 v206, v78
	v_mov_b32_e32 v207, v77
	v_pk_add_f32 v[204:205], v[204:205], v[206:207]
	v_pk_mov_b32 v[206:207], v[90:91], v[88:89] op_sel:[1,0]
	v_mov_b32_e32 v208, v90
	v_mov_b32_e32 v209, v89
	v_pk_add_f32 v[206:207], v[206:207], v[208:209]
	v_pk_mov_b32 v[208:209], v[94:95], v[92:93] op_sel:[1,0]
	v_mov_b32_e32 v210, v94
	v_mov_b32_e32 v211, v93
	v_pk_add_f32 v[208:209], v[208:209], v[210:211]
	v_add_f32_e32 v203, v204, v205
	v_pk_add_f32 v[208:209], v[208:209], v[208:209] op_sel_hi:[0,1]
	v_pk_mov_b32 v[210:211], v[98:99], v[96:97] op_sel:[1,0]
	v_mov_b32_e32 v212, v98
	v_mov_b32_e32 v213, v97
	v_add_f32_e32 v205, 0, v203
	v_pk_add_f32 v[210:211], v[210:211], v[212:213]
	v_add_f32_e32 v213, v172, v173
	v_add_f32_e32 v215, v164, v165
	v_mov_b32_e32 v212, v182
	v_mov_b32_e32 v214, v183
	v_mov_b32_e32 v208, v178
	v_mov_b32_e32 v204, v179
	v_pk_add_f32 v[212:213], v[212:213], v[214:215]
	v_pk_add_f32 v[204:205], v[208:209], v[204:205]
	v_add_f32_e32 v203, v206, v207
	v_pk_add_f32 v[204:205], v[212:213], v[204:205]
	v_add_f32_e32 v207, 0, v203
	v_add_f32_e32 v203, v204, v205
	v_pk_add_f32 v[210:211], v[210:211], v[210:211] op_sel_hi:[0,1]
	v_add_f32_e32 v217, v176, v177
	v_add_f32_dpp v203, v203, v203 quad_perm:[1,0,3,2] row_mask:0xf bank_mask:0xf bound_ctrl:1
	v_add_f32_e32 v219, v174, v175
	v_mov_b32_e32 v216, v184
	v_add_f32_dpp v203, v203, v203 quad_perm:[2,3,0,1] row_mask:0xf bank_mask:0xf bound_ctrl:1
	v_mov_b32_e32 v218, v185
	v_mov_b32_e32 v210, v180
	v_mov_b32_e32 v206, v181
	v_add_f32_dpp v203, v203, v203 row_half_mirror row_mask:0xf bank_mask:0xf bound_ctrl:1
	v_pk_add_f32 v[204:205], v[216:217], v[218:219]
	v_pk_add_f32 v[206:207], v[210:211], v[206:207]
	v_add_f32_dpp v203, v203, v203 row_mirror row_mask:0xf bank_mask:0xf bound_ctrl:1
	v_pk_add_f32 v[204:205], v[204:205], v[206:207]
	v_readlane_b32 s4, v203, 16
	v_readlane_b32 s5, v203, 48
	v_add_f32_e32 v206, v204, v205
	v_readlane_b32 s0, v203, 0
	v_readlane_b32 s1, v203, 32
	v_mov_b32_e32 v204, s4
	v_mov_b32_e32 v205, s5
	v_pk_add_f32 v[204:205], s[0:1], v[204:205]
	s_nop 0
	v_add_f32_e32 v203, v204, v205
	v_add_f32_dpp v204, v206, v206 quad_perm:[1,0,3,2] row_mask:0xf bank_mask:0xf bound_ctrl:1
	v_fmamk_f32 v79, v203, 0xba800000, v79
	v_fmac_f32_e32 v78, 0xba800000, v203
	v_add_f32_dpp v204, v204, v204 quad_perm:[2,3,0,1] row_mask:0xf bank_mask:0xf bound_ctrl:1
	v_fmamk_f32 v77, v203, 0xba800000, v77
	v_fmac_f32_e32 v76, 0xba800000, v203
	v_add_f32_dpp v204, v204, v204 row_half_mirror row_mask:0xf bank_mask:0xf bound_ctrl:1
	v_pk_mul_f32 v[206:207], v[78:79], v[78:79]
	v_fmamk_f32 v95, v203, 0xba800000, v95
	v_add_f32_dpp v204, v204, v204 row_mirror row_mask:0xf bank_mask:0xf bound_ctrl:1
	v_fmac_f32_e32 v94, 0xba800000, v203
	v_readlane_b32 s4, v204, 16
	v_readlane_b32 s5, v204, 48
	v_readlane_b32 s0, v204, 0
	v_readlane_b32 s1, v204, 32
	v_mov_b32_e32 v204, s4
	v_mov_b32_e32 v205, s5
	v_pk_add_f32 v[204:205], s[0:1], v[204:205]
	v_fmamk_f32 v93, v203, 0xba800000, v93
	v_add_f32_e32 v220, v204, v205
	v_pk_mul_f32 v[204:205], v[76:77], v[76:77]
	v_fmamk_f32 v91, v220, 0xba800000, v91
	v_fmac_f32_e32 v90, 0xba800000, v220
	v_fmamk_f32 v89, v220, 0xba800000, v89
	v_fmac_f32_e32 v88, 0xba800000, v220
	v_pk_mov_b32 v[208:209], v[206:207], v[204:205] op_sel:[1,0]
	v_mov_b32_e32 v207, v205
	v_pk_add_f32 v[204:205], v[208:209], v[206:207]
	v_pk_mul_f32 v[206:207], v[88:89], v[88:89]
	v_pk_mul_f32 v[208:209], v[90:91], v[90:91]
	v_fmac_f32_e32 v92, 0xba800000, v203
	v_pk_mov_b32 v[210:211], v[208:209], v[206:207] op_sel:[1,0]
	v_mov_b32_e32 v209, v207
	v_pk_add_f32 v[206:207], v[210:211], v[208:209]
	v_pk_mul_f32 v[208:209], v[92:93], v[92:93]
	v_pk_mul_f32 v[210:211], v[94:95], v[94:95]
	v_fmamk_f32 v99, v220, 0xba800000, v99
	v_fmac_f32_e32 v98, 0xba800000, v220
	v_fmamk_f32 v97, v220, 0xba800000, v97
	v_fmac_f32_e32 v96, 0xba800000, v220
	v_pk_mov_b32 v[212:213], v[210:211], v[208:209] op_sel:[1,0]
	v_mov_b32_e32 v211, v209
	v_pk_add_f32 v[204:205], v[204:205], v[204:205] op_sel_hi:[0,1]
	v_pk_add_f32 v[208:209], v[212:213], v[210:211]
	v_pk_mul_f32 v[210:211], v[96:97], v[96:97]
	v_pk_mul_f32 v[212:213], v[98:99], v[98:99]
	v_fmac_f32_e32 v172, 0xba800000, v203
	v_pk_mov_b32 v[214:215], v[212:213], v[210:211] op_sel:[1,0]
	v_mov_b32_e32 v213, v211
	v_fmamk_f32 v173, v203, 0xba800000, v173
	v_fmac_f32_e32 v164, 0xba800000, v203
	v_mul_f32_e32 v204, v172, v172
	v_pk_add_f32 v[210:211], v[214:215], v[212:213]
	v_fmamk_f32 v165, v203, 0xba800000, v165
	v_fmac_f32_e32 v176, 0xba800000, v220
	v_pk_fma_f32 v[212:213], v[172:173], v[172:173], v[204:205] op_sel_hi:[1,1,0]
	v_mul_f32_e32 v204, v164, v164
	v_fmamk_f32 v177, v220, 0xba800000, v177
	v_fmac_f32_e32 v174, 0xba800000, v220
	v_pk_fma_f32 v[214:215], v[164:165], v[164:165], v[204:205] op_sel_hi:[1,1,0]
	v_mul_f32_e32 v204, v176, v176
	v_pk_add_f32 v[208:209], v[208:209], v[208:209] op_sel_hi:[0,1]
	v_fmamk_f32 v175, v220, 0xba800000, v175
	v_pk_fma_f32 v[216:217], v[176:177], v[176:177], v[204:205] op_sel_hi:[1,1,0]
	v_mul_f32_e32 v204, v174, v174
	v_fmamk_f32 v179, v203, 0xba800000, v179
	v_fmac_f32_e32 v178, 0xba800000, v203
	v_fmamk_f32 v183, v203, 0xba800000, v183
	v_fmac_f32_e32 v182, 0xba800000, v203
	v_pk_fma_f32 v[218:219], v[174:175], v[174:175], v[204:205] op_sel_hi:[1,1,0]
	v_mul_f32_e32 v212, v182, v182
	v_mul_f32_e32 v214, v183, v183
	v_mul_f32_e32 v204, v178, v178
	v_mul_f32_e32 v208, v179, v179
	v_pk_add_f32 v[212:213], v[212:213], v[214:215]
	v_pk_add_f32 v[204:205], v[204:205], v[208:209]
	v_pk_add_f32 v[206:207], v[206:207], v[206:207] op_sel_hi:[0,1]
	v_pk_add_f32 v[204:205], v[212:213], v[204:205]
	v_pk_add_f32 v[210:211], v[210:211], v[210:211] op_sel_hi:[0,1]
	v_add_f32_e32 v203, v204, v205
	v_fmamk_f32 v181, v220, 0xba800000, v181
	v_fmac_f32_e32 v180, 0xba800000, v220
	v_add_f32_dpp v203, v203, v203 quad_perm:[1,0,3,2] row_mask:0xf bank_mask:0xf bound_ctrl:1
	v_fmamk_f32 v185, v220, 0xba800000, v185
	v_fmac_f32_e32 v184, 0xba800000, v220
	v_add_f32_dpp v203, v203, v203 quad_perm:[2,3,0,1] row_mask:0xf bank_mask:0xf bound_ctrl:1
	v_mul_f32_e32 v216, v184, v184
	v_mul_f32_e32 v218, v185, v185
	v_mul_f32_e32 v206, v180, v180
	v_mul_f32_e32 v210, v181, v181
	v_add_f32_dpp v203, v203, v203 row_half_mirror row_mask:0xf bank_mask:0xf bound_ctrl:1
	v_pk_add_f32 v[204:205], v[216:217], v[218:219]
	v_pk_add_f32 v[206:207], v[206:207], v[210:211]
	v_add_f32_dpp v203, v203, v203 row_mirror row_mask:0xf bank_mask:0xf bound_ctrl:1
	v_pk_add_f32 v[204:205], v[204:205], v[206:207]
	v_readlane_b32 s4, v203, 16
	v_readlane_b32 s5, v203, 48
	v_add_f32_e32 v206, v204, v205
	v_readlane_b32 s0, v203, 0
	v_readlane_b32 s1, v203, 32
	v_mov_b32_e32 v204, s4
	v_mov_b32_e32 v205, s5
	v_pk_add_f32 v[204:205], s[0:1], v[204:205]
	s_nop 0
	v_add_f32_e32 v203, v204, v205
	v_add_f32_dpp v204, v206, v206 quad_perm:[1,0,3,2] row_mask:0xf bank_mask:0xf bound_ctrl:1
	v_fmamk_f32 v203, v203, 0x3a800000, v190
	v_rsq_f32_e32 v206, v203
	v_add_f32_dpp v204, v204, v204 quad_perm:[2,3,0,1] row_mask:0xf bank_mask:0xf bound_ctrl:1
	v_pk_mul_f32 v[78:79], v[78:79], v[206:207] op_sel_hi:[1,0]
	s_nop 0
	v_add_f32_dpp v204, v204, v204 row_half_mirror row_mask:0xf bank_mask:0xf bound_ctrl:1
	v_pk_mul_f32 v[76:77], v[76:77], v[206:207] op_sel_hi:[1,0]
	v_pk_mul_f32 v[92:93], v[92:93], v[206:207] op_sel_hi:[1,0]
	v_add_f32_dpp v204, v204, v204 row_mirror row_mask:0xf bank_mask:0xf bound_ctrl:1
	v_pk_fma_f32 v[208:209], v[76:77], v[4:5], v[12:13]
	v_readlane_b32 s4, v204, 16
	v_readlane_b32 s5, v204, 48
	v_readlane_b32 s0, v204, 0
	v_readlane_b32 s1, v204, 32
	v_mov_b32_e32 v204, s4
	v_mov_b32_e32 v205, s5
	v_pk_add_f32 v[204:205], s[0:1], v[204:205]
	v_pk_fma_f32 v[76:77], v[78:79], v[2:3], v[10:11]
	v_add_f32_e32 v203, v204, v205
	v_fmamk_f32 v203, v203, 0x3a800000, v190
	v_rsq_f32_e32 v204, v203
	v_pk_mul_f32 v[164:165], v[164:165], v[206:207] op_sel_hi:[1,0]
	v_pk_fma_f32 v[92:93], v[92:93], v[8:9], v[16:17]
	v_pk_fma_f32 v[164:165], v[164:165], v[20:21], v[28:29]
	v_pk_mul_f32 v[78:79], v[90:91], v[204:205] op_sel_hi:[1,0]
	v_pk_mul_f32 v[88:89], v[88:89], v[204:205] op_sel_hi:[1,0]
	v_pk_mul_f32 v[90:91], v[94:95], v[206:207] op_sel_hi:[1,0]
	v_pk_mul_f32 v[94:95], v[98:99], v[204:205] op_sel_hi:[1,0]
	v_pk_mul_f32 v[98:99], v[172:173], v[206:207] op_sel_hi:[1,0]
	v_pk_mul_f32 v[172:173], v[176:177], v[204:205] op_sel_hi:[1,0]
	v_pk_fma_f32 v[88:89], v[4:5], v[88:89], v[12:13]
	v_pk_fma_f32 v[78:79], v[2:3], v[78:79], v[10:11]
	v_pk_fma_f32 v[90:91], v[90:91], v[6:7], v[14:15]
	v_pk_fma_f32 v[94:95], v[6:7], v[94:95], v[14:15]
	v_pk_fma_f32 v[172:173], v[18:19], v[172:173], v[26:27]
	v_cvt_pk_bf16_f32 v78, v78, v79
	v_cvt_pk_bf16_f32 v79, v88, v89
	v_cvt_pk_bf16_f32 v88, v90, v91
	v_cvt_pk_bf16_f32 v89, v92, v93
	v_cvt_pk_bf16_f32 v90, v94, v95
	v_cvt_pk_bf16_f32 v93, v164, v165
	v_cvt_pk_bf16_f32 v94, v172, v173
	s_waitcnt vmcnt(47)
	v_lshlrev_b32_e32 v164, 16, v158
	v_and_b32_e32 v165, 0xffff0000, v158
	v_lshlrev_b32_e32 v158, 16, v159
	v_and_b32_e32 v159, 0xffff0000, v159
	s_waitcnt vmcnt(43)
	v_lshlrev_b32_e32 v172, 16, v162
	v_and_b32_e32 v173, 0xffff0000, v162
	v_lshlrev_b32_e32 v162, 16, v163
	v_and_b32_e32 v163, 0xffff0000, v163
	v_pk_fma_f32 v[158:159], v[158:159], s[96:97], v[162:163] op_sel_hi:[1,0,1]
	v_pk_fma_f32 v[162:163], v[164:165], s[96:97], v[172:173] op_sel_hi:[1,0,1]
	s_waitcnt vmcnt(39)
	v_lshlrev_b32_e32 v164, 16, v156
	v_and_b32_e32 v165, 0xffff0000, v156
	v_lshlrev_b32_e32 v156, 16, v157
	v_and_b32_e32 v157, 0xffff0000, v157
	s_waitcnt vmcnt(35)
	v_lshlrev_b32_e32 v172, 16, v160
	v_and_b32_e32 v173, 0xffff0000, v160
	v_lshlrev_b32_e32 v160, 16, v161
	v_and_b32_e32 v161, 0xffff0000, v161
	v_pk_fma_f32 v[156:157], v[156:157], s[96:97], v[160:161] op_sel_hi:[1,0,1]
	v_pk_fma_f32 v[160:161], v[164:165], s[96:97], v[172:173] op_sel_hi:[1,0,1]
	v_lshlrev_b32_e32 v164, 16, v150
	v_and_b32_e32 v165, 0xffff0000, v150
	v_lshlrev_b32_e32 v150, 16, v151
	v_and_b32_e32 v151, 0xffff0000, v151
	v_lshlrev_b32_e32 v172, 16, v154
	v_and_b32_e32 v173, 0xffff0000, v154
	v_lshlrev_b32_e32 v154, 16, v155
	v_and_b32_e32 v155, 0xffff0000, v155
	v_pk_fma_f32 v[150:151], v[150:151], s[96:97], v[154:155] op_sel_hi:[1,0,1]
	v_pk_fma_f32 v[154:155], v[164:165], s[96:97], v[172:173] op_sel_hi:[1,0,1]
	v_lshlrev_b32_e32 v164, 16, v148
	v_and_b32_e32 v165, 0xffff0000, v148
	v_lshlrev_b32_e32 v148, 16, v149
	v_and_b32_e32 v149, 0xffff0000, v149
	s_waitcnt vmcnt(34)
	v_lshlrev_b32_e32 v172, 16, v152
	v_and_b32_e32 v173, 0xffff0000, v152
	v_lshlrev_b32_e32 v152, 16, v153
	v_and_b32_e32 v153, 0xffff0000, v153
	v_pk_fma_f32 v[148:149], v[148:149], s[96:97], v[152:153] op_sel_hi:[1,0,1]
	v_pk_fma_f32 v[152:153], v[164:165], s[96:97], v[172:173] op_sel_hi:[1,0,1]
	v_lshlrev_b32_e32 v164, 16, v144
	v_and_b32_e32 v165, 0xffff0000, v144
	v_lshlrev_b32_e32 v144, 16, v145
	v_and_b32_e32 v145, 0xffff0000, v145
	v_lshlrev_b32_e32 v172, 16, v146
	v_and_b32_e32 v173, 0xffff0000, v146
	v_lshlrev_b32_e32 v146, 16, v147
	v_and_b32_e32 v147, 0xffff0000, v147
	v_pk_fma_f32 v[144:145], v[144:145], s[96:97], v[146:147] op_sel_hi:[1,0,1]
	v_pk_fma_f32 v[146:147], v[164:165], s[96:97], v[172:173] op_sel_hi:[1,0,1]
	v_lshlrev_b32_e32 v164, 16, v140
	v_and_b32_e32 v165, 0xffff0000, v140
	v_lshlrev_b32_e32 v140, 16, v141
	v_and_b32_e32 v141, 0xffff0000, v141
	s_waitcnt vmcnt(33)
	v_lshlrev_b32_e32 v172, 16, v142
	v_and_b32_e32 v173, 0xffff0000, v142
	v_lshlrev_b32_e32 v142, 16, v143
	v_and_b32_e32 v143, 0xffff0000, v143
	v_pk_fma_f32 v[140:141], v[140:141], s[96:97], v[142:143] op_sel_hi:[1,0,1]
	v_pk_fma_f32 v[142:143], v[164:165], s[96:97], v[172:173] op_sel_hi:[1,0,1]
	v_lshlrev_b32_e32 v164, 16, v136
	v_and_b32_e32 v165, 0xffff0000, v136
	v_lshlrev_b32_e32 v136, 16, v137
	v_and_b32_e32 v137, 0xffff0000, v137
	v_lshlrev_b32_e32 v172, 16, v138
	v_and_b32_e32 v173, 0xffff0000, v138
	v_lshlrev_b32_e32 v138, 16, v139
	v_and_b32_e32 v139, 0xffff0000, v139
	v_pk_mul_f32 v[174:175], v[174:175], v[204:205] op_sel_hi:[1,0]
	v_pk_fma_f32 v[136:137], v[136:137], s[96:97], v[138:139] op_sel_hi:[1,0,1]
	v_pk_fma_f32 v[138:139], v[164:165], s[96:97], v[172:173] op_sel_hi:[1,0,1]
	v_lshlrev_b32_e32 v164, 16, v132
	v_and_b32_e32 v165, 0xffff0000, v132
	v_lshlrev_b32_e32 v132, 16, v133
	v_and_b32_e32 v133, 0xffff0000, v133
	s_waitcnt vmcnt(32)
	v_lshlrev_b32_e32 v172, 16, v134
	v_and_b32_e32 v173, 0xffff0000, v134
	v_lshlrev_b32_e32 v134, 16, v135
	v_and_b32_e32 v135, 0xffff0000, v135
	v_pk_mul_f32 v[96:97], v[96:97], v[204:205] op_sel_hi:[1,0]
	v_pk_fma_f32 v[174:175], v[20:21], v[174:175], v[28:29]
	v_pk_mul_f32 v[176:177], v[182:183], v[206:207] op_sel_hi:[1,0]
	v_pk_fma_f32 v[132:133], v[132:133], s[96:97], v[134:135] op_sel_hi:[1,0,1]
	v_pk_fma_f32 v[134:135], v[164:165], s[96:97], v[172:173] op_sel_hi:[1,0,1]
	v_pk_mov_b32 v[164:165], v[162:163], v[158:159] op_sel:[1,0]
	v_mov_b32_e32 v172, v162
	v_mov_b32_e32 v173, v159
	v_pk_fma_f32 v[96:97], v[8:9], v[96:97], v[16:17]
	v_pk_fma_f32 v[176:177], v[176:177], v[22:23], v[30:31]
	v_cvt_pk_bf16_f32 v95, v174, v175
	v_pk_add_f32 v[164:165], v[164:165], v[172:173]
	v_pk_mov_b32 v[172:173], v[160:161], v[156:157] op_sel:[1,0]
	v_mov_b32_e32 v174, v160
	v_mov_b32_e32 v175, v157
	v_pk_mul_f32 v[178:179], v[178:179], v[206:207] op_sel_hi:[1,0]
	v_cvt_pk_bf16_f32 v91, v96, v97
	v_cvt_pk_bf16_f32 v96, v176, v177
	v_pk_add_f32 v[172:173], v[172:173], v[174:175]
	v_pk_mov_b32 v[174:175], v[154:155], v[150:151] op_sel:[1,0]
	v_mov_b32_e32 v176, v154
	v_mov_b32_e32 v177, v151
	v_pk_fma_f32 v[178:179], v[178:179], v[24:25], v[32:33]
	v_pk_mul_f32 v[180:181], v[180:181], v[204:205] op_sel_hi:[1,0]
	v_add_f32_e32 v164, v164, v165
	v_pk_add_f32 v[174:175], v[174:175], v[176:177]
	v_pk_fma_f32 v[98:99], v[98:99], v[18:19], v[26:27]
	v_pk_fma_f32 v[180:181], v[24:25], v[180:181], v[32:33]
	v_readlane_b32 s0, v238, 16
	v_cvt_pk_bf16_f32 v97, v178, v179
	v_add_f32_e32 v165, 0, v164
	v_add_f32_e32 v164, v172, v173
	v_pk_add_f32 v[174:175], v[174:175], v[174:175] op_sel_hi:[0,1]
	v_pk_mov_b32 v[176:177], v[152:153], v[148:149] op_sel:[1,0]
	v_mov_b32_e32 v178, v152
	v_mov_b32_e32 v179, v149
	v_pk_mul_f32 v[182:183], v[184:185], v[204:205] op_sel_hi:[1,0]
	v_readlane_b32 s1, v238, 17
	v_cvt_pk_bf16_f32 v92, v98, v99
	v_cvt_pk_bf16_f32 v99, v180, v181
	v_add_f32_e32 v173, 0, v164
	v_pk_add_f32 v[176:177], v[176:177], v[178:179]
	v_add_f32_e32 v179, v146, v147
	v_add_f32_e32 v181, v144, v145
	v_mov_b32_e32 v178, v138
	v_mov_b32_e32 v180, v139
	v_mov_b32_e32 v174, v136
	v_mov_b32_e32 v164, v137
	v_pk_fma_f32 v[182:183], v[22:23], v[182:183], v[30:31]
	v_lshl_add_u64 v[184:185], v[50:51], 0, s[0:1]
	v_cvt_pk_bf16_f32 v76, v76, v77
	v_cvt_pk_bf16_f32 v77, v208, v209
	v_pk_add_f32 v[176:177], v[176:177], v[176:177] op_sel_hi:[0,1]
	v_pk_add_f32 v[178:179], v[178:179], v[180:181]
	v_pk_add_f32 v[164:165], v[174:175], v[164:165]
	global_store_dwordx2 v[184:185], v[76:77], off
	global_store_dwordx2 v[184:185], v[78:79], off offset:2048
	global_store_dwordx2 v[184:185], v[88:89], off offset:512
	global_store_dwordx2 v[184:185], v[90:91], off offset:2560
	global_store_dwordx2 v[184:185], v[92:93], off offset:1024
	global_store_dwordx2 v[184:185], v[94:95], off offset:3072
	v_cvt_pk_bf16_f32 v98, v182, v183
	global_store_dwordx2 v[184:185], v[96:97], off offset:1536
	global_store_dwordx2 v[184:185], v[98:99], off offset:3584
	v_add_f32_e32 v183, v142, v143
	v_add_f32_e32 v185, v140, v141
	v_pk_add_f32 v[164:165], v[178:179], v[164:165]
	v_mov_b32_e32 v182, v134
	v_mov_b32_e32 v184, v135
	v_mov_b32_e32 v176, v132
	v_mov_b32_e32 v172, v133
	v_add_f32_e32 v174, v164, v165
	v_pk_add_f32 v[164:165], v[182:183], v[184:185]
	v_pk_add_f32 v[172:173], v[176:177], v[172:173]
	s_nop 0
	v_pk_add_f32 v[164:165], v[164:165], v[172:173]
	s_nop 0
	v_add_f32_e32 v172, v164, v165
	v_add_f32_dpp v164, v174, v174 quad_perm:[1,0,3,2] row_mask:0xf bank_mask:0xf bound_ctrl:1
	s_nop 1
	v_add_f32_dpp v164, v164, v164 quad_perm:[2,3,0,1] row_mask:0xf bank_mask:0xf bound_ctrl:1
	s_nop 1
	v_add_f32_dpp v164, v164, v164 row_half_mirror row_mask:0xf bank_mask:0xf bound_ctrl:1
	s_nop 1
	v_add_f32_dpp v164, v164, v164 row_mirror row_mask:0xf bank_mask:0xf bound_ctrl:1
	s_nop 0
	v_readlane_b32 s4, v164, 16
	v_readlane_b32 s5, v164, 48
	v_readlane_b32 s0, v164, 0
	v_readlane_b32 s1, v164, 32
	v_mov_b32_e32 v164, s4
	v_mov_b32_e32 v165, s5
	v_pk_add_f32 v[164:165], s[0:1], v[164:165]
	s_nop 0
	v_add_f32_e32 v203, v164, v165
	v_add_f32_dpp v164, v172, v172 quad_perm:[1,0,3,2] row_mask:0xf bank_mask:0xf bound_ctrl:1
	v_fmamk_f32 v163, v203, 0xba800000, v163
	v_fmac_f32_e32 v162, 0xba800000, v203
	v_add_f32_dpp v164, v164, v164 quad_perm:[2,3,0,1] row_mask:0xf bank_mask:0xf bound_ctrl:1
	v_fmamk_f32 v159, v203, 0xba800000, v159
	v_fmac_f32_e32 v158, 0xba800000, v203
	v_add_f32_dpp v164, v164, v164 row_half_mirror row_mask:0xf bank_mask:0xf bound_ctrl:1
	v_pk_mul_f32 v[172:173], v[162:163], v[162:163]
	v_fmamk_f32 v155, v203, 0xba800000, v155
	v_add_f32_dpp v164, v164, v164 row_mirror row_mask:0xf bank_mask:0xf bound_ctrl:1
	v_fmac_f32_e32 v154, 0xba800000, v203
	v_readlane_b32 s4, v164, 16
	v_readlane_b32 s5, v164, 48
	v_readlane_b32 s0, v164, 0
	v_readlane_b32 s1, v164, 32
	v_mov_b32_e32 v164, s4
	v_mov_b32_e32 v165, s5
	v_pk_add_f32 v[164:165], s[0:1], v[164:165]
	v_fmamk_f32 v151, v203, 0xba800000, v151
	v_add_f32_e32 v204, v164, v165
	v_pk_mul_f32 v[164:165], v[158:159], v[158:159]
	v_fmamk_f32 v161, v204, 0xba800000, v161
	v_fmac_f32_e32 v160, 0xba800000, v204
	v_fmamk_f32 v157, v204, 0xba800000, v157
	v_fmac_f32_e32 v156, 0xba800000, v204
	v_pk_mov_b32 v[174:175], v[172:173], v[164:165] op_sel:[1,0]
	v_mov_b32_e32 v173, v165
	v_pk_add_f32 v[164:165], v[174:175], v[172:173]
	v_pk_mul_f32 v[172:173], v[156:157], v[156:157]
	v_pk_mul_f32 v[174:175], v[160:161], v[160:161]
	v_fmac_f32_e32 v150, 0xba800000, v203
	v_pk_mov_b32 v[176:177], v[174:175], v[172:173] op_sel:[1,0]
	v_mov_b32_e32 v175, v173
	v_pk_add_f32 v[172:173], v[176:177], v[174:175]
	v_pk_mul_f32 v[174:175], v[150:151], v[150:151]
	v_pk_mul_f32 v[176:177], v[154:155], v[154:155]
	v_fmamk_f32 v153, v204, 0xba800000, v153
	v_fmac_f32_e32 v152, 0xba800000, v204
	v_fmamk_f32 v149, v204, 0xba800000, v149
	v_fmac_f32_e32 v148, 0xba800000, v204
	v_pk_mov_b32 v[178:179], v[176:177], v[174:175] op_sel:[1,0]
	v_mov_b32_e32 v177, v175
	v_pk_add_f32 v[164:165], v[164:165], v[164:165] op_sel_hi:[0,1]
	v_pk_add_f32 v[174:175], v[178:179], v[176:177]
	v_pk_mul_f32 v[176:177], v[148:149], v[148:149]
	v_pk_mul_f32 v[178:179], v[152:153], v[152:153]
	v_fmac_f32_e32 v146, 0xba800000, v203
	v_pk_mov_b32 v[180:181], v[178:179], v[176:177] op_sel:[1,0]
	v_mov_b32_e32 v179, v177
	v_fmamk_f32 v147, v203, 0xba800000, v147
	v_fmac_f32_e32 v144, 0xba800000, v203
	v_mul_f32_e32 v164, v146, v146
	v_pk_add_f32 v[176:177], v[180:181], v[178:179]
	v_fmamk_f32 v145, v203, 0xba800000, v145
	v_fmac_f32_e32 v142, 0xba800000, v204
	v_pk_fma_f32 v[178:179], v[146:147], v[146:147], v[164:165] op_sel_hi:[1,1,0]
	v_mul_f32_e32 v164, v144, v144
	v_fmamk_f32 v143, v204, 0xba800000, v143
	v_fmac_f32_e32 v140, 0xba800000, v204
	v_pk_fma_f32 v[180:181], v[144:145], v[144:145], v[164:165] op_sel_hi:[1,1,0]
	v_mul_f32_e32 v164, v142, v142
	v_pk_add_f32 v[174:175], v[174:175], v[174:175] op_sel_hi:[0,1]
	v_fmamk_f32 v141, v204, 0xba800000, v141
	v_pk_fma_f32 v[182:183], v[142:143], v[142:143], v[164:165] op_sel_hi:[1,1,0]
	v_mul_f32_e32 v164, v140, v140
	v_fmamk_f32 v137, v203, 0xba800000, v137
	v_fmac_f32_e32 v136, 0xba800000, v203
	v_fmamk_f32 v139, v203, 0xba800000, v139
	v_fmac_f32_e32 v138, 0xba800000, v203
	v_pk_fma_f32 v[184:185], v[140:141], v[140:141], v[164:165] op_sel_hi:[1,1,0]
	v_mul_f32_e32 v178, v138, v138
	v_mul_f32_e32 v180, v139, v139
	v_mul_f32_e32 v164, v136, v136
	v_mul_f32_e32 v174, v137, v137
	v_pk_add_f32 v[172:173], v[172:173], v[172:173] op_sel_hi:[0,1]
	v_pk_add_f32 v[176:177], v[176:177], v[176:177] op_sel_hi:[0,1]
	v_fmamk_f32 v133, v204, 0xba800000, v133
	v_fmac_f32_e32 v132, 0xba800000, v204
	v_fmamk_f32 v135, v204, 0xba800000, v135
	v_fmac_f32_e32 v134, 0xba800000, v204
	v_pk_add_f32 v[178:179], v[178:179], v[180:181]
	v_pk_add_f32 v[164:165], v[164:165], v[174:175]
	v_mul_f32_e32 v182, v134, v134
	v_pk_add_f32 v[164:165], v[178:179], v[164:165]
	v_mul_f32_e32 v184, v135, v135
	v_mul_f32_e32 v172, v132, v132
	v_mul_f32_e32 v176, v133, v133
	v_add_f32_e32 v174, v164, v165
	v_pk_add_f32 v[164:165], v[182:183], v[184:185]
	v_pk_add_f32 v[172:173], v[172:173], v[176:177]
	s_nop 0
	v_pk_add_f32 v[164:165], v[164:165], v[172:173]
	s_nop 0
	v_add_f32_e32 v172, v164, v165
	v_add_f32_dpp v164, v174, v174 quad_perm:[1,0,3,2] row_mask:0xf bank_mask:0xf bound_ctrl:1
	s_nop 1
	v_add_f32_dpp v164, v164, v164 quad_perm:[2,3,0,1] row_mask:0xf bank_mask:0xf bound_ctrl:1
	s_nop 1
	v_add_f32_dpp v164, v164, v164 row_half_mirror row_mask:0xf bank_mask:0xf bound_ctrl:1
	s_nop 1
	v_add_f32_dpp v164, v164, v164 row_mirror row_mask:0xf bank_mask:0xf bound_ctrl:1
	s_nop 0
	v_readlane_b32 s4, v164, 16
	v_readlane_b32 s5, v164, 48
	v_readlane_b32 s0, v164, 0
	v_readlane_b32 s1, v164, 32
	v_mov_b32_e32 v164, s4
	v_mov_b32_e32 v165, s5
	v_pk_add_f32 v[164:165], s[0:1], v[164:165]
	s_nop 0
	v_add_f32_e32 v173, v164, v165
	v_add_f32_dpp v164, v172, v172 quad_perm:[1,0,3,2] row_mask:0xf bank_mask:0xf bound_ctrl:1
	v_fmamk_f32 v172, v173, 0x3a800000, v190
	v_rsq_f32_e32 v172, v172
	v_add_f32_dpp v164, v164, v164 quad_perm:[2,3,0,1] row_mask:0xf bank_mask:0xf bound_ctrl:1
	v_pk_mul_f32 v[150:151], v[150:151], v[172:173] op_sel_hi:[1,0]
	s_nop 0
	v_add_f32_dpp v164, v164, v164 row_half_mirror row_mask:0xf bank_mask:0xf bound_ctrl:1
	v_pk_fma_f32 v[150:151], v[150:151], v[8:9], v[16:17]
	v_pk_mul_f32 v[138:139], v[138:139], v[172:173] op_sel_hi:[1,0]
	v_add_f32_dpp v164, v164, v164 row_mirror row_mask:0xf bank_mask:0xf bound_ctrl:1
	v_pk_mul_f32 v[136:137], v[136:137], v[172:173] op_sel_hi:[1,0]
	v_readlane_b32 s4, v164, 16
	v_readlane_b32 s5, v164, 48
	v_readlane_b32 s0, v164, 0
	v_readlane_b32 s1, v164, 32
	v_mov_b32_e32 v164, s4
	v_mov_b32_e32 v165, s5
	v_pk_add_f32 v[164:165], s[0:1], v[164:165]
	v_pk_mul_f32 v[162:163], v[162:163], v[172:173] op_sel_hi:[1,0]
	v_add_f32_e32 v164, v164, v165
	v_fmamk_f32 v164, v164, 0x3a800000, v190
	v_rsq_f32_e32 v164, v164
	v_pk_mul_f32 v[158:159], v[158:159], v[172:173] op_sel_hi:[1,0]
	v_pk_mul_f32 v[154:155], v[154:155], v[172:173] op_sel_hi:[1,0]
	v_pk_mul_f32 v[146:147], v[146:147], v[172:173] op_sel_hi:[1,0]
	v_pk_mul_f32 v[148:149], v[148:149], v[164:165] op_sel_hi:[1,0]
	v_pk_mul_f32 v[144:145], v[144:145], v[172:173] op_sel_hi:[1,0]
	v_pk_fma_f32 v[148:149], v[8:9], v[148:149], v[16:17]
	v_pk_fma_f32 v[172:173], v[136:137], v[24:25], v[32:33]
	v_pk_fma_f32 v[176:177], v[138:139], v[22:23], v[30:31]
	v_cvt_pk_bf16_f32 v137, v150, v151
	v_cvt_pk_bf16_f32 v139, v148, v149
	s_waitcnt vmcnt(39)
	v_lshlrev_b32_e32 v148, 16, v126
	v_and_b32_e32 v149, 0xffff0000, v126
	v_lshlrev_b32_e32 v126, 16, v127
	v_and_b32_e32 v127, 0xffff0000, v127
	s_waitcnt vmcnt(35)
	v_lshlrev_b32_e32 v150, 16, v130
	v_and_b32_e32 v151, 0xffff0000, v130
	v_lshlrev_b32_e32 v130, 16, v131
	v_and_b32_e32 v131, 0xffff0000, v131
	v_pk_fma_f32 v[126:127], v[126:127], s[96:97], v[130:131] op_sel_hi:[1,0,1]
	v_pk_fma_f32 v[130:131], v[148:149], s[96:97], v[150:151] op_sel_hi:[1,0,1]
	s_waitcnt vmcnt(31)
	v_lshlrev_b32_e32 v148, 16, v124
	v_and_b32_e32 v149, 0xffff0000, v124
	v_lshlrev_b32_e32 v124, 16, v125
	v_and_b32_e32 v125, 0xffff0000, v125
	s_waitcnt vmcnt(27)
	v_lshlrev_b32_e32 v150, 16, v128
	v_and_b32_e32 v151, 0xffff0000, v128
	v_lshlrev_b32_e32 v128, 16, v129
	v_and_b32_e32 v129, 0xffff0000, v129
	v_pk_fma_f32 v[124:125], v[124:125], s[96:97], v[128:129] op_sel_hi:[1,0,1]
	v_pk_fma_f32 v[128:129], v[148:149], s[96:97], v[150:151] op_sel_hi:[1,0,1]
	v_lshlrev_b32_e32 v148, 16, v118
	v_and_b32_e32 v149, 0xffff0000, v118
	v_lshlrev_b32_e32 v118, 16, v119
	v_and_b32_e32 v119, 0xffff0000, v119
	v_lshlrev_b32_e32 v150, 16, v122
	v_and_b32_e32 v151, 0xffff0000, v122
	v_lshlrev_b32_e32 v122, 16, v123
	v_and_b32_e32 v123, 0xffff0000, v123
	v_pk_fma_f32 v[118:119], v[118:119], s[96:97], v[122:123] op_sel_hi:[1,0,1]
	v_pk_fma_f32 v[122:123], v[148:149], s[96:97], v[150:151] op_sel_hi:[1,0,1]
	v_lshlrev_b32_e32 v148, 16, v116
	v_and_b32_e32 v149, 0xffff0000, v116
	v_lshlrev_b32_e32 v116, 16, v117
	v_and_b32_e32 v117, 0xffff0000, v117
	s_waitcnt vmcnt(26)
	v_lshlrev_b32_e32 v150, 16, v120
	v_and_b32_e32 v151, 0xffff0000, v120
	v_lshlrev_b32_e32 v120, 16, v121
	v_and_b32_e32 v121, 0xffff0000, v121
	v_pk_fma_f32 v[116:117], v[116:117], s[96:97], v[120:121] op_sel_hi:[1,0,1]
	v_pk_fma_f32 v[120:121], v[148:149], s[96:97], v[150:151] op_sel_hi:[1,0,1]
	v_lshlrev_b32_e32 v148, 16, v112
	v_and_b32_e32 v149, 0xffff0000, v112
	v_lshlrev_b32_e32 v112, 16, v113
	v_and_b32_e32 v113, 0xffff0000, v113
	v_lshlrev_b32_e32 v150, 16, v114
	v_and_b32_e32 v151, 0xffff0000, v114
	v_lshlrev_b32_e32 v114, 16, v115
	v_and_b32_e32 v115, 0xffff0000, v115
	v_pk_fma_f32 v[112:113], v[112:113], s[96:97], v[114:115] op_sel_hi:[1,0,1]
	v_pk_fma_f32 v[114:115], v[148:149], s[96:97], v[150:151] op_sel_hi:[1,0,1]
	v_lshlrev_b32_e32 v148, 16, v108
	v_and_b32_e32 v149, 0xffff0000, v108
	v_lshlrev_b32_e32 v108, 16, v109
	v_and_b32_e32 v109, 0xffff0000, v109
	s_waitcnt vmcnt(25)
	v_lshlrev_b32_e32 v150, 16, v110
	v_and_b32_e32 v151, 0xffff0000, v110
	v_lshlrev_b32_e32 v110, 16, v111
	v_and_b32_e32 v111, 0xffff0000, v111
	v_pk_fma_f32 v[108:109], v[108:109], s[96:97], v[110:111] op_sel_hi:[1,0,1]
	v_pk_fma_f32 v[110:111], v[148:149], s[96:97], v[150:151] op_sel_hi:[1,0,1]
	v_lshlrev_b32_e32 v148, 16, v104
	v_and_b32_e32 v149, 0xffff0000, v104
	v_lshlrev_b32_e32 v104, 16, v105
	v_and_b32_e32 v105, 0xffff0000, v105
	v_lshlrev_b32_e32 v150, 16, v106
	v_and_b32_e32 v151, 0xffff0000, v106
	v_lshlrev_b32_e32 v106, 16, v107
	v_and_b32_e32 v107, 0xffff0000, v107
	v_pk_mul_f32 v[152:153], v[152:153], v[164:165] op_sel_hi:[1,0]
	v_pk_fma_f32 v[104:105], v[104:105], s[96:97], v[106:107] op_sel_hi:[1,0,1]
	v_pk_fma_f32 v[106:107], v[148:149], s[96:97], v[150:151] op_sel_hi:[1,0,1]
	v_lshlrev_b32_e32 v148, 16, v100
	v_and_b32_e32 v149, 0xffff0000, v100
	v_lshlrev_b32_e32 v100, 16, v101
	v_and_b32_e32 v101, 0xffff0000, v101
	s_waitcnt vmcnt(24)
	v_lshlrev_b32_e32 v150, 16, v102
	v_and_b32_e32 v151, 0xffff0000, v102
	v_lshlrev_b32_e32 v102, 16, v103
	v_and_b32_e32 v103, 0xffff0000, v103
	v_pk_fma_f32 v[152:153], v[6:7], v[152:153], v[14:15]
	v_pk_fma_f32 v[100:101], v[100:101], s[96:97], v[102:103] op_sel_hi:[1,0,1]
	v_pk_fma_f32 v[102:103], v[148:149], s[96:97], v[150:151] op_sel_hi:[1,0,1]
	v_pk_mov_b32 v[148:149], v[130:131], v[126:127] op_sel:[1,0]
	v_mov_b32_e32 v150, v130
	v_mov_b32_e32 v151, v127
	v_pk_fma_f32 v[154:155], v[154:155], v[6:7], v[14:15]
	v_cvt_pk_bf16_f32 v138, v152, v153
	v_pk_add_f32 v[148:149], v[148:149], v[150:151]
	v_pk_mov_b32 v[150:151], v[128:129], v[124:125] op_sel:[1,0]
	v_mov_b32_e32 v152, v128
	v_mov_b32_e32 v153, v125
	v_pk_mul_f32 v[156:157], v[156:157], v[164:165] op_sel_hi:[1,0]
	v_cvt_pk_bf16_f32 v136, v154, v155
	v_pk_add_f32 v[150:151], v[150:151], v[152:153]
	v_pk_mov_b32 v[152:153], v[122:123], v[118:119] op_sel:[1,0]
	v_mov_b32_e32 v154, v122
	v_mov_b32_e32 v155, v119
	v_pk_fma_f32 v[156:157], v[4:5], v[156:157], v[12:13]
	v_pk_mul_f32 v[134:135], v[134:135], v[164:165] op_sel_hi:[1,0]
	v_add_f32_e32 v148, v148, v149
	v_pk_add_f32 v[152:153], v[152:153], v[154:155]
	v_pk_fma_f32 v[158:159], v[158:159], v[4:5], v[12:13]
	v_pk_mul_f32 v[132:133], v[132:133], v[164:165] op_sel_hi:[1,0]
	v_pk_fma_f32 v[178:179], v[22:23], v[134:135], v[30:31]
	v_cvt_pk_bf16_f32 v135, v156, v157
	v_add_f32_e32 v149, 0, v148
	v_add_f32_e32 v148, v150, v151
	v_pk_add_f32 v[152:153], v[152:153], v[152:153] op_sel_hi:[0,1]
	v_pk_mov_b32 v[154:155], v[120:121], v[116:117] op_sel:[1,0]
	v_mov_b32_e32 v156, v120
	v_mov_b32_e32 v157, v117
	v_pk_mul_f32 v[160:161], v[160:161], v[164:165] op_sel_hi:[1,0]
	v_pk_mul_f32 v[142:143], v[142:143], v[164:165] op_sel_hi:[1,0]
	v_pk_mul_f32 v[140:141], v[140:141], v[164:165] op_sel_hi:[1,0]
	v_pk_fma_f32 v[164:165], v[24:25], v[132:133], v[32:33]
	v_cvt_pk_bf16_f32 v133, v158, v159
	v_add_f32_e32 v151, 0, v148
	v_pk_add_f32 v[154:155], v[154:155], v[156:157]
	v_add_f32_e32 v157, v114, v115
	v_add_f32_e32 v159, v112, v113
	v_mov_b32_e32 v156, v106
	v_mov_b32_e32 v158, v107
	v_mov_b32_e32 v152, v104
	v_mov_b32_e32 v148, v105
	v_pk_fma_f32 v[162:163], v[162:163], v[2:3], v[10:11]
	v_pk_fma_f32 v[160:161], v[2:3], v[160:161], v[10:11]
	v_pk_add_f32 v[154:155], v[154:155], v[154:155] op_sel_hi:[0,1]
	v_pk_add_f32 v[156:157], v[156:157], v[158:159]
	v_pk_add_f32 v[148:149], v[152:153], v[148:149]
	v_cvt_pk_bf16_f32 v132, v162, v163
	v_cvt_pk_bf16_f32 v134, v160, v161
	v_add_f32_e32 v161, v110, v111
	v_add_f32_e32 v163, v108, v109
	v_pk_add_f32 v[148:149], v[156:157], v[148:149]
	v_mov_b32_e32 v160, v102
	v_mov_b32_e32 v162, v103
	v_mov_b32_e32 v154, v100
	v_mov_b32_e32 v150, v101
	v_add_f32_e32 v152, v148, v149
	v_pk_add_f32 v[148:149], v[160:161], v[162:163]
	v_pk_add_f32 v[150:151], v[154:155], v[150:151]
	v_readlane_b32 s0, v239, 32
	v_pk_add_f32 v[148:149], v[148:149], v[150:151]
	v_readlane_b32 s1, v239, 33
	v_add_f32_e32 v150, v148, v149
	v_add_f32_dpp v148, v152, v152 quad_perm:[1,0,3,2] row_mask:0xf bank_mask:0xf bound_ctrl:1
	v_lshl_add_u64 v[180:181], v[50:51], 0, s[0:1]
	v_pk_fma_f32 v[146:147], v[146:147], v[18:19], v[26:27]
	v_add_f32_dpp v148, v148, v148 quad_perm:[2,3,0,1] row_mask:0xf bank_mask:0xf bound_ctrl:1
	v_pk_fma_f32 v[174:175], v[20:21], v[140:141], v[28:29]
	v_cvt_pk_bf16_f32 v140, v146, v147
	v_add_f32_dpp v148, v148, v148 row_half_mirror row_mask:0xf bank_mask:0xf bound_ctrl:1
	v_cvt_pk_bf16_f32 v147, v164, v165
	v_pk_fma_f32 v[144:145], v[144:145], v[20:21], v[28:29]
	v_add_f32_dpp v148, v148, v148 row_mirror row_mask:0xf bank_mask:0xf bound_ctrl:1
	v_pk_fma_f32 v[142:143], v[18:19], v[142:143], v[26:27]
	v_readlane_b32 s4, v148, 16
	v_readlane_b32 s5, v148, 48
	v_readlane_b32 s0, v148, 0
	v_readlane_b32 s1, v148, 32
	v_mov_b32_e32 v148, s4
	v_mov_b32_e32 v149, s5
	v_pk_add_f32 v[148:149], s[0:1], v[148:149]
	v_cvt_pk_bf16_f32 v141, v144, v145
	v_add_f32_e32 v164, v148, v149
	v_add_f32_dpp v148, v150, v150 quad_perm:[1,0,3,2] row_mask:0xf bank_mask:0xf bound_ctrl:1
	v_fmamk_f32 v131, v164, 0xba800000, v131
	v_fmac_f32_e32 v130, 0xba800000, v164
	v_add_f32_dpp v148, v148, v148 quad_perm:[2,3,0,1] row_mask:0xf bank_mask:0xf bound_ctrl:1
	v_fmamk_f32 v127, v164, 0xba800000, v127
	v_fmac_f32_e32 v126, 0xba800000, v164
	v_add_f32_dpp v148, v148, v148 row_half_mirror row_mask:0xf bank_mask:0xf bound_ctrl:1
	v_pk_mul_f32 v[150:151], v[130:131], v[130:131]
	v_fmamk_f32 v123, v164, 0xba800000, v123
	v_add_f32_dpp v148, v148, v148 row_mirror row_mask:0xf bank_mask:0xf bound_ctrl:1
	v_fmac_f32_e32 v122, 0xba800000, v164
	v_readlane_b32 s4, v148, 16
	v_readlane_b32 s5, v148, 48
	v_readlane_b32 s0, v148, 0
	v_readlane_b32 s1, v148, 32
	v_mov_b32_e32 v148, s4
	v_mov_b32_e32 v149, s5
	v_pk_add_f32 v[148:149], s[0:1], v[148:149]
	v_fmamk_f32 v119, v164, 0xba800000, v119
	v_add_f32_e32 v165, v148, v149
	v_pk_mul_f32 v[148:149], v[126:127], v[126:127]
	v_fmamk_f32 v129, v165, 0xba800000, v129
	v_fmac_f32_e32 v128, 0xba800000, v165
	v_fmamk_f32 v125, v165, 0xba800000, v125
	v_fmac_f32_e32 v124, 0xba800000, v165
	v_pk_mov_b32 v[152:153], v[150:151], v[148:149] op_sel:[1,0]
	v_mov_b32_e32 v151, v149
	v_pk_add_f32 v[148:149], v[152:153], v[150:151]
	v_pk_mul_f32 v[150:151], v[124:125], v[124:125]
	v_pk_mul_f32 v[152:153], v[128:129], v[128:129]
	v_fmac_f32_e32 v118, 0xba800000, v164
	v_pk_mov_b32 v[154:155], v[152:153], v[150:151] op_sel:[1,0]
	v_mov_b32_e32 v153, v151
	v_pk_add_f32 v[150:151], v[154:155], v[152:153]
	v_pk_mul_f32 v[152:153], v[118:119], v[118:119]
	v_pk_mul_f32 v[154:155], v[122:123], v[122:123]
	v_fmamk_f32 v121, v165, 0xba800000, v121
	v_fmac_f32_e32 v120, 0xba800000, v165
	v_fmamk_f32 v117, v165, 0xba800000, v117
	v_fmac_f32_e32 v116, 0xba800000, v165
	v_pk_mov_b32 v[156:157], v[154:155], v[152:153] op_sel:[1,0]
	v_mov_b32_e32 v155, v153
	v_pk_add_f32 v[148:149], v[148:149], v[148:149] op_sel_hi:[0,1]
	v_pk_add_f32 v[152:153], v[156:157], v[154:155]
	v_pk_mul_f32 v[154:155], v[116:117], v[116:117]
	v_pk_mul_f32 v[156:157], v[120:121], v[120:121]
	v_fmac_f32_e32 v114, 0xba800000, v164
	v_pk_mov_b32 v[158:159], v[156:157], v[154:155] op_sel:[1,0]
	v_mov_b32_e32 v157, v155
	v_fmamk_f32 v115, v164, 0xba800000, v115
	v_fmac_f32_e32 v112, 0xba800000, v164
	v_mul_f32_e32 v148, v114, v114
	v_pk_add_f32 v[154:155], v[158:159], v[156:157]
	v_fmamk_f32 v113, v164, 0xba800000, v113
	v_fmac_f32_e32 v110, 0xba800000, v165
	v_pk_fma_f32 v[156:157], v[114:115], v[114:115], v[148:149] op_sel_hi:[1,1,0]
	v_mul_f32_e32 v148, v112, v112
	v_fmamk_f32 v111, v165, 0xba800000, v111
	v_fmac_f32_e32 v108, 0xba800000, v165
	v_pk_fma_f32 v[158:159], v[112:113], v[112:113], v[148:149] op_sel_hi:[1,1,0]
	v_mul_f32_e32 v148, v110, v110
	v_pk_add_f32 v[152:153], v[152:153], v[152:153] op_sel_hi:[0,1]
	v_fmamk_f32 v109, v165, 0xba800000, v109
	v_pk_fma_f32 v[160:161], v[110:111], v[110:111], v[148:149] op_sel_hi:[1,1,0]
	v_mul_f32_e32 v148, v108, v108
	v_fmamk_f32 v105, v164, 0xba800000, v105
	v_fmac_f32_e32 v104, 0xba800000, v164
	v_fmamk_f32 v107, v164, 0xba800000, v107
	v_fmac_f32_e32 v106, 0xba800000, v164
	v_pk_fma_f32 v[162:163], v[108:109], v[108:109], v[148:149] op_sel_hi:[1,1,0]
	v_mul_f32_e32 v156, v106, v106
	v_mul_f32_e32 v158, v107, v107
	v_mul_f32_e32 v148, v104, v104
	v_mul_f32_e32 v152, v105, v105
	v_pk_add_f32 v[150:151], v[150:151], v[150:151] op_sel_hi:[0,1]
	v_pk_add_f32 v[154:155], v[154:155], v[154:155] op_sel_hi:[0,1]
	v_fmamk_f32 v101, v165, 0xba800000, v101
	v_fmac_f32_e32 v100, 0xba800000, v165
	v_fmamk_f32 v103, v165, 0xba800000, v103
	v_fmac_f32_e32 v102, 0xba800000, v165
	v_pk_add_f32 v[156:157], v[156:157], v[158:159]
	v_pk_add_f32 v[148:149], v[148:149], v[152:153]
	v_mul_f32_e32 v160, v102, v102
	v_pk_add_f32 v[148:149], v[156:157], v[148:149]
	v_mul_f32_e32 v162, v103, v103
	v_mul_f32_e32 v150, v100, v100
	v_mul_f32_e32 v154, v101, v101
	v_add_f32_e32 v152, v148, v149
	v_pk_add_f32 v[148:149], v[160:161], v[162:163]
	v_pk_add_f32 v[150:151], v[150:151], v[154:155]
	v_cvt_pk_bf16_f32 v144, v176, v177
	v_pk_add_f32 v[148:149], v[148:149], v[150:151]
	v_cvt_pk_bf16_f32 v145, v172, v173
	v_add_f32_e32 v150, v148, v149
	v_add_f32_dpp v148, v152, v152 quad_perm:[1,0,3,2] row_mask:0xf bank_mask:0xf bound_ctrl:1
	global_store_dwordx2 v[180:181], v[132:133], off
	global_store_dwordx2 v[180:181], v[134:135], off offset:2048
	v_add_f32_dpp v148, v148, v148 quad_perm:[2,3,0,1] row_mask:0xf bank_mask:0xf bound_ctrl:1
	global_store_dwordx2 v[180:181], v[136:137], off offset:512
	global_store_dwordx2 v[180:181], v[138:139], off offset:2560
	v_add_f32_dpp v148, v148, v148 row_half_mirror row_mask:0xf bank_mask:0xf bound_ctrl:1
	v_cvt_pk_bf16_f32 v142, v142, v143
	v_cvt_pk_bf16_f32 v143, v174, v175
	v_add_f32_dpp v148, v148, v148 row_mirror row_mask:0xf bank_mask:0xf bound_ctrl:1
	global_store_dwordx2 v[180:181], v[140:141], off offset:1024
	global_store_dwordx2 v[180:181], v[142:143], off offset:3072
	v_readlane_b32 s4, v148, 16
	v_readlane_b32 s5, v148, 48
	v_readlane_b32 s0, v148, 0
	v_readlane_b32 s1, v148, 32
	v_mov_b32_e32 v148, s4
	v_mov_b32_e32 v149, s5
	v_pk_add_f32 v[148:149], s[0:1], v[148:149]
	v_cvt_pk_bf16_f32 v146, v178, v179
	v_add_f32_e32 v151, v148, v149
	v_add_f32_dpp v148, v150, v150 quad_perm:[1,0,3,2] row_mask:0xf bank_mask:0xf bound_ctrl:1
	v_fmamk_f32 v150, v151, 0x3a800000, v190
	v_rsq_f32_e32 v150, v150
	v_add_f32_dpp v148, v148, v148 quad_perm:[2,3,0,1] row_mask:0xf bank_mask:0xf bound_ctrl:1
	global_store_dwordx2 v[180:181], v[144:145], off offset:1536
	global_store_dwordx2 v[180:181], v[146:147], off offset:3584
	v_add_f32_dpp v148, v148, v148 row_half_mirror row_mask:0xf bank_mask:0xf bound_ctrl:1
	v_pk_mul_f32 v[118:119], v[118:119], v[150:151] op_sel_hi:[1,0]
	v_pk_mul_f32 v[106:107], v[106:107], v[150:151] op_sel_hi:[1,0]
	v_add_f32_dpp v148, v148, v148 row_mirror row_mask:0xf bank_mask:0xf bound_ctrl:1
	v_pk_fma_f32 v[118:119], v[118:119], v[8:9], v[16:17]
	v_readlane_b32 s4, v148, 16
	v_readlane_b32 s5, v148, 48
	v_readlane_b32 s0, v148, 0
	v_readlane_b32 s1, v148, 32
	v_mov_b32_e32 v148, s4
	v_mov_b32_e32 v149, s5
	v_pk_add_f32 v[148:149], s[0:1], v[148:149]
	v_pk_mul_f32 v[104:105], v[104:105], v[150:151] op_sel_hi:[1,0]
	v_add_f32_e32 v148, v148, v149
	v_fmamk_f32 v148, v148, 0x3a800000, v190
	v_rsq_f32_e32 v148, v148
	v_pk_mul_f32 v[130:131], v[130:131], v[150:151] op_sel_hi:[1,0]
	v_pk_mul_f32 v[126:127], v[126:127], v[150:151] op_sel_hi:[1,0]
	v_pk_mul_f32 v[122:123], v[122:123], v[150:151] op_sel_hi:[1,0]
	v_pk_mul_f32 v[116:117], v[116:117], v[148:149] op_sel_hi:[1,0]
	v_pk_mul_f32 v[114:115], v[114:115], v[150:151] op_sel_hi:[1,0]
	v_pk_fma_f32 v[116:117], v[8:9], v[116:117], v[16:17]
	v_pk_mul_f32 v[112:113], v[112:113], v[150:151] op_sel_hi:[1,0]
	v_pk_fma_f32 v[150:151], v[104:105], v[24:25], v[32:33]
	v_pk_fma_f32 v[154:155], v[106:107], v[22:23], v[30:31]
	v_cvt_pk_bf16_f32 v105, v118, v119
	v_cvt_pk_bf16_f32 v107, v116, v117
	s_waitcnt vmcnt(31)
	v_lshlrev_b32_e32 v116, 16, v82
	v_and_b32_e32 v117, 0xffff0000, v82
	v_lshlrev_b32_e32 v82, 16, v83
	v_and_b32_e32 v83, 0xffff0000, v83
	s_waitcnt vmcnt(27)
	v_lshlrev_b32_e32 v118, 16, v86
	v_and_b32_e32 v119, 0xffff0000, v86
	v_lshlrev_b32_e32 v86, 16, v87
	v_and_b32_e32 v87, 0xffff0000, v87
	v_pk_fma_f32 v[82:83], v[82:83], s[96:97], v[86:87] op_sel_hi:[1,0,1]
	v_pk_fma_f32 v[86:87], v[116:117], s[96:97], v[118:119] op_sel_hi:[1,0,1]
	s_waitcnt vmcnt(23)
	v_lshlrev_b32_e32 v116, 16, v80
	v_and_b32_e32 v117, 0xffff0000, v80
	v_lshlrev_b32_e32 v80, 16, v81
	v_and_b32_e32 v81, 0xffff0000, v81
	s_waitcnt vmcnt(19)
	v_lshlrev_b32_e32 v118, 16, v84
	v_and_b32_e32 v119, 0xffff0000, v84
	v_lshlrev_b32_e32 v84, 16, v85
	v_and_b32_e32 v85, 0xffff0000, v85
	v_pk_fma_f32 v[80:81], v[80:81], s[96:97], v[84:85] op_sel_hi:[1,0,1]
	v_pk_fma_f32 v[84:85], v[116:117], s[96:97], v[118:119] op_sel_hi:[1,0,1]
	v_lshlrev_b32_e32 v116, 16, v70
	v_and_b32_e32 v117, 0xffff0000, v70
	v_lshlrev_b32_e32 v70, 16, v71
	v_and_b32_e32 v71, 0xffff0000, v71
	v_lshlrev_b32_e32 v118, 16, v74
	v_and_b32_e32 v119, 0xffff0000, v74
	v_lshlrev_b32_e32 v74, 16, v75
	v_and_b32_e32 v75, 0xffff0000, v75
	v_pk_fma_f32 v[70:71], v[70:71], s[96:97], v[74:75] op_sel_hi:[1,0,1]
	v_pk_fma_f32 v[74:75], v[116:117], s[96:97], v[118:119] op_sel_hi:[1,0,1]
	v_lshlrev_b32_e32 v116, 16, v68
	v_and_b32_e32 v117, 0xffff0000, v68
	v_lshlrev_b32_e32 v68, 16, v69
	v_and_b32_e32 v69, 0xffff0000, v69
	s_waitcnt vmcnt(18)
	v_lshlrev_b32_e32 v118, 16, v72
	v_and_b32_e32 v119, 0xffff0000, v72
	v_lshlrev_b32_e32 v72, 16, v73
	v_and_b32_e32 v73, 0xffff0000, v73
	v_pk_fma_f32 v[68:69], v[68:69], s[96:97], v[72:73] op_sel_hi:[1,0,1]
	v_pk_fma_f32 v[72:73], v[116:117], s[96:97], v[118:119] op_sel_hi:[1,0,1]
	v_lshlrev_b32_e32 v116, 16, v64
	v_and_b32_e32 v117, 0xffff0000, v64
	v_lshlrev_b32_e32 v64, 16, v65
	v_and_b32_e32 v65, 0xffff0000, v65
	v_lshlrev_b32_e32 v118, 16, v66
	v_and_b32_e32 v119, 0xffff0000, v66
	v_lshlrev_b32_e32 v66, 16, v67
	v_and_b32_e32 v67, 0xffff0000, v67
	v_pk_fma_f32 v[64:65], v[64:65], s[96:97], v[66:67] op_sel_hi:[1,0,1]
	v_pk_fma_f32 v[66:67], v[116:117], s[96:97], v[118:119] op_sel_hi:[1,0,1]
	v_lshlrev_b32_e32 v116, 16, v60
	v_and_b32_e32 v117, 0xffff0000, v60
	v_lshlrev_b32_e32 v60, 16, v61
	v_and_b32_e32 v61, 0xffff0000, v61
	s_waitcnt vmcnt(17)
	v_lshlrev_b32_e32 v118, 16, v62
	v_and_b32_e32 v119, 0xffff0000, v62
	v_lshlrev_b32_e32 v62, 16, v63
	v_and_b32_e32 v63, 0xffff0000, v63
	v_pk_fma_f32 v[60:61], v[60:61], s[96:97], v[62:63] op_sel_hi:[1,0,1]
	v_pk_fma_f32 v[62:63], v[116:117], s[96:97], v[118:119] op_sel_hi:[1,0,1]
	v_lshlrev_b32_e32 v116, 16, v56
	v_and_b32_e32 v117, 0xffff0000, v56
	v_lshlrev_b32_e32 v56, 16, v57
	v_and_b32_e32 v57, 0xffff0000, v57
	v_lshlrev_b32_e32 v118, 16, v58
	v_and_b32_e32 v119, 0xffff0000, v58
	v_lshlrev_b32_e32 v58, 16, v59
	v_and_b32_e32 v59, 0xffff0000, v59
	v_pk_mul_f32 v[120:121], v[120:121], v[148:149] op_sel_hi:[1,0]
	v_pk_fma_f32 v[56:57], v[56:57], s[96:97], v[58:59] op_sel_hi:[1,0,1]
	v_pk_fma_f32 v[58:59], v[116:117], s[96:97], v[118:119] op_sel_hi:[1,0,1]
	v_lshlrev_b32_e32 v116, 16, v52
	v_and_b32_e32 v117, 0xffff0000, v52
	v_lshlrev_b32_e32 v52, 16, v53
	v_and_b32_e32 v53, 0xffff0000, v53
	s_waitcnt vmcnt(16)
	v_lshlrev_b32_e32 v118, 16, v54
	v_and_b32_e32 v119, 0xffff0000, v54
	v_lshlrev_b32_e32 v54, 16, v55
	v_and_b32_e32 v55, 0xffff0000, v55
	v_pk_fma_f32 v[120:121], v[6:7], v[120:121], v[14:15]
	v_pk_fma_f32 v[52:53], v[52:53], s[96:97], v[54:55] op_sel_hi:[1,0,1]
	v_pk_fma_f32 v[54:55], v[116:117], s[96:97], v[118:119] op_sel_hi:[1,0,1]
	v_pk_mov_b32 v[116:117], v[86:87], v[82:83] op_sel:[1,0]
	v_mov_b32_e32 v118, v86
	v_mov_b32_e32 v119, v83
	v_pk_fma_f32 v[122:123], v[122:123], v[6:7], v[14:15]
	v_cvt_pk_bf16_f32 v106, v120, v121
	v_pk_add_f32 v[116:117], v[116:117], v[118:119]
	v_pk_mov_b32 v[118:119], v[84:85], v[80:81] op_sel:[1,0]
	v_mov_b32_e32 v120, v84
	v_mov_b32_e32 v121, v81
	v_pk_mul_f32 v[124:125], v[124:125], v[148:149] op_sel_hi:[1,0]
	v_cvt_pk_bf16_f32 v104, v122, v123
	v_pk_add_f32 v[118:119], v[118:119], v[120:121]
	v_pk_mov_b32 v[120:121], v[74:75], v[70:71] op_sel:[1,0]
	v_mov_b32_e32 v122, v74
	v_mov_b32_e32 v123, v71
	v_pk_fma_f32 v[124:125], v[4:5], v[124:125], v[12:13]
	v_pk_mul_f32 v[102:103], v[102:103], v[148:149] op_sel_hi:[1,0]
	v_add_f32_e32 v116, v116, v117
	v_pk_add_f32 v[120:121], v[120:121], v[122:123]
	v_pk_fma_f32 v[126:127], v[126:127], v[4:5], v[12:13]
	v_pk_mul_f32 v[100:101], v[100:101], v[148:149] op_sel_hi:[1,0]
	v_pk_fma_f32 v[156:157], v[22:23], v[102:103], v[30:31]
	v_cvt_pk_bf16_f32 v103, v124, v125
	v_add_f32_e32 v117, 0, v116
	v_add_f32_e32 v116, v118, v119
	v_pk_add_f32 v[120:121], v[120:121], v[120:121] op_sel_hi:[0,1]
	v_pk_mov_b32 v[122:123], v[72:73], v[68:69] op_sel:[1,0]
	v_mov_b32_e32 v124, v72
	v_mov_b32_e32 v125, v69
	v_pk_mul_f32 v[128:129], v[128:129], v[148:149] op_sel_hi:[1,0]
	v_pk_mul_f32 v[110:111], v[110:111], v[148:149] op_sel_hi:[1,0]
	v_pk_mul_f32 v[108:109], v[108:109], v[148:149] op_sel_hi:[1,0]
	v_pk_fma_f32 v[148:149], v[24:25], v[100:101], v[32:33]
	v_cvt_pk_bf16_f32 v101, v126, v127
	v_add_f32_e32 v119, 0, v116
	v_pk_add_f32 v[122:123], v[122:123], v[124:125]
	v_add_f32_e32 v125, v66, v67
	v_add_f32_e32 v127, v64, v65
	v_mov_b32_e32 v124, v58
	v_mov_b32_e32 v126, v59
	v_mov_b32_e32 v120, v56
	v_mov_b32_e32 v116, v57
	v_pk_fma_f32 v[130:131], v[130:131], v[2:3], v[10:11]
	v_pk_fma_f32 v[128:129], v[2:3], v[128:129], v[10:11]
	v_pk_add_f32 v[122:123], v[122:123], v[122:123] op_sel_hi:[0,1]
	v_pk_add_f32 v[124:125], v[124:125], v[126:127]
	v_pk_add_f32 v[116:117], v[120:121], v[116:117]
	v_cvt_pk_bf16_f32 v100, v130, v131
	v_cvt_pk_bf16_f32 v102, v128, v129
	v_add_f32_e32 v129, v62, v63
	v_add_f32_e32 v131, v60, v61
	v_pk_add_f32 v[116:117], v[124:125], v[116:117]
	v_mov_b32_e32 v128, v54
	v_mov_b32_e32 v130, v55
	v_mov_b32_e32 v122, v52
	v_mov_b32_e32 v118, v53
	v_add_f32_e32 v120, v116, v117
	v_pk_add_f32 v[116:117], v[128:129], v[130:131]
	v_pk_add_f32 v[118:119], v[122:123], v[118:119]
	v_readlane_b32 s0, v239, 34
	v_pk_add_f32 v[116:117], v[116:117], v[118:119]
	v_readlane_b32 s1, v239, 35
	v_add_f32_e32 v118, v116, v117
	v_add_f32_dpp v116, v120, v120 quad_perm:[1,0,3,2] row_mask:0xf bank_mask:0xf bound_ctrl:1
	v_lshl_add_u64 v[158:159], v[50:51], 0, s[0:1]
	v_pk_fma_f32 v[114:115], v[114:115], v[18:19], v[26:27]
	v_add_f32_dpp v116, v116, v116 quad_perm:[2,3,0,1] row_mask:0xf bank_mask:0xf bound_ctrl:1
	v_pk_fma_f32 v[152:153], v[20:21], v[108:109], v[28:29]
	v_cvt_pk_bf16_f32 v108, v114, v115
	v_add_f32_dpp v116, v116, v116 row_half_mirror row_mask:0xf bank_mask:0xf bound_ctrl:1
	v_cvt_pk_bf16_f32 v115, v148, v149
	v_pk_fma_f32 v[112:113], v[112:113], v[20:21], v[28:29]
	v_add_f32_dpp v116, v116, v116 row_mirror row_mask:0xf bank_mask:0xf bound_ctrl:1
	v_pk_fma_f32 v[110:111], v[18:19], v[110:111], v[26:27]
	v_readlane_b32 s4, v116, 16
	v_readlane_b32 s5, v116, 48
	v_readlane_b32 s0, v116, 0
	v_readlane_b32 s1, v116, 32
	v_mov_b32_e32 v116, s4
	v_mov_b32_e32 v117, s5
	v_pk_add_f32 v[116:117], s[0:1], v[116:117]
	v_cvt_pk_bf16_f32 v109, v112, v113
	v_add_f32_e32 v148, v116, v117
	v_add_f32_dpp v116, v118, v118 quad_perm:[1,0,3,2] row_mask:0xf bank_mask:0xf bound_ctrl:1
	v_fmamk_f32 v87, v148, 0xba800000, v87
	v_fmac_f32_e32 v86, 0xba800000, v148
	v_add_f32_dpp v116, v116, v116 quad_perm:[2,3,0,1] row_mask:0xf bank_mask:0xf bound_ctrl:1
	v_fmamk_f32 v83, v148, 0xba800000, v83
	v_fmac_f32_e32 v82, 0xba800000, v148
	v_add_f32_dpp v116, v116, v116 row_half_mirror row_mask:0xf bank_mask:0xf bound_ctrl:1
	v_pk_mul_f32 v[118:119], v[86:87], v[86:87]
	v_fmamk_f32 v75, v148, 0xba800000, v75
	v_add_f32_dpp v116, v116, v116 row_mirror row_mask:0xf bank_mask:0xf bound_ctrl:1
	v_fmac_f32_e32 v74, 0xba800000, v148
	v_readlane_b32 s4, v116, 16
	v_readlane_b32 s5, v116, 48
	v_readlane_b32 s0, v116, 0
	v_readlane_b32 s1, v116, 32
	v_mov_b32_e32 v116, s4
	v_mov_b32_e32 v117, s5
	v_pk_add_f32 v[116:117], s[0:1], v[116:117]
	v_fmamk_f32 v71, v148, 0xba800000, v71
	v_add_f32_e32 v149, v116, v117
	v_pk_mul_f32 v[116:117], v[82:83], v[82:83]
	v_fmamk_f32 v85, v149, 0xba800000, v85
	v_fmac_f32_e32 v84, 0xba800000, v149
	v_fmamk_f32 v81, v149, 0xba800000, v81
	v_fmac_f32_e32 v80, 0xba800000, v149
	v_pk_mov_b32 v[120:121], v[118:119], v[116:117] op_sel:[1,0]
	v_mov_b32_e32 v119, v117
	v_pk_add_f32 v[116:117], v[120:121], v[118:119]
	v_pk_mul_f32 v[118:119], v[80:81], v[80:81]
	v_pk_mul_f32 v[120:121], v[84:85], v[84:85]
	v_fmac_f32_e32 v70, 0xba800000, v148
	v_pk_mov_b32 v[122:123], v[120:121], v[118:119] op_sel:[1,0]
	v_mov_b32_e32 v121, v119
	v_pk_add_f32 v[118:119], v[122:123], v[120:121]
	v_pk_mul_f32 v[120:121], v[70:71], v[70:71]
	v_pk_mul_f32 v[122:123], v[74:75], v[74:75]
	v_fmamk_f32 v73, v149, 0xba800000, v73
	v_fmac_f32_e32 v72, 0xba800000, v149
	v_fmamk_f32 v69, v149, 0xba800000, v69
	v_fmac_f32_e32 v68, 0xba800000, v149
	v_pk_mov_b32 v[124:125], v[122:123], v[120:121] op_sel:[1,0]
	v_mov_b32_e32 v123, v121
	v_pk_add_f32 v[116:117], v[116:117], v[116:117] op_sel_hi:[0,1]
	v_pk_add_f32 v[120:121], v[124:125], v[122:123]
	v_pk_mul_f32 v[122:123], v[68:69], v[68:69]
	v_pk_mul_f32 v[124:125], v[72:73], v[72:73]
	v_fmac_f32_e32 v66, 0xba800000, v148
	v_pk_mov_b32 v[126:127], v[124:125], v[122:123] op_sel:[1,0]
	v_mov_b32_e32 v125, v123
	v_fmamk_f32 v67, v148, 0xba800000, v67
	v_fmac_f32_e32 v64, 0xba800000, v148
	v_mul_f32_e32 v116, v66, v66
	v_pk_add_f32 v[122:123], v[126:127], v[124:125]
	v_fmamk_f32 v65, v148, 0xba800000, v65
	v_fmac_f32_e32 v62, 0xba800000, v149
	v_pk_fma_f32 v[124:125], v[66:67], v[66:67], v[116:117] op_sel_hi:[1,1,0]
	v_mul_f32_e32 v116, v64, v64
	v_fmamk_f32 v63, v149, 0xba800000, v63
	v_fmac_f32_e32 v60, 0xba800000, v149
	v_pk_fma_f32 v[126:127], v[64:65], v[64:65], v[116:117] op_sel_hi:[1,1,0]
	v_mul_f32_e32 v116, v62, v62
	v_pk_add_f32 v[120:121], v[120:121], v[120:121] op_sel_hi:[0,1]
	v_fmamk_f32 v61, v149, 0xba800000, v61
	v_pk_fma_f32 v[128:129], v[62:63], v[62:63], v[116:117] op_sel_hi:[1,1,0]
	v_mul_f32_e32 v116, v60, v60
	v_fmamk_f32 v57, v148, 0xba800000, v57
	v_fmac_f32_e32 v56, 0xba800000, v148
	v_fmamk_f32 v59, v148, 0xba800000, v59
	v_fmac_f32_e32 v58, 0xba800000, v148
	v_pk_fma_f32 v[130:131], v[60:61], v[60:61], v[116:117] op_sel_hi:[1,1,0]
	v_mul_f32_e32 v124, v58, v58
	v_mul_f32_e32 v126, v59, v59
	v_mul_f32_e32 v116, v56, v56
	v_mul_f32_e32 v120, v57, v57
	v_pk_add_f32 v[118:119], v[118:119], v[118:119] op_sel_hi:[0,1]
	v_pk_add_f32 v[122:123], v[122:123], v[122:123] op_sel_hi:[0,1]
	v_fmamk_f32 v53, v149, 0xba800000, v53
	v_fmac_f32_e32 v52, 0xba800000, v149
	v_fmamk_f32 v55, v149, 0xba800000, v55
	v_fmac_f32_e32 v54, 0xba800000, v149
	v_pk_add_f32 v[124:125], v[124:125], v[126:127]
	v_pk_add_f32 v[116:117], v[116:117], v[120:121]
	v_mul_f32_e32 v128, v54, v54
	v_pk_add_f32 v[116:117], v[124:125], v[116:117]
	v_mul_f32_e32 v130, v55, v55
	v_mul_f32_e32 v118, v52, v52
	v_mul_f32_e32 v122, v53, v53
	v_add_f32_e32 v120, v116, v117
	v_pk_add_f32 v[116:117], v[128:129], v[130:131]
	v_pk_add_f32 v[118:119], v[118:119], v[122:123]
	v_cvt_pk_bf16_f32 v112, v154, v155
	v_pk_add_f32 v[116:117], v[116:117], v[118:119]
	v_cvt_pk_bf16_f32 v113, v150, v151
	v_add_f32_e32 v118, v116, v117
	v_add_f32_dpp v116, v120, v120 quad_perm:[1,0,3,2] row_mask:0xf bank_mask:0xf bound_ctrl:1
	global_store_dwordx2 v[158:159], v[100:101], off
	global_store_dwordx2 v[158:159], v[102:103], off offset:2048
	v_add_f32_dpp v116, v116, v116 quad_perm:[2,3,0,1] row_mask:0xf bank_mask:0xf bound_ctrl:1
	global_store_dwordx2 v[158:159], v[104:105], off offset:512
	global_store_dwordx2 v[158:159], v[106:107], off offset:2560
	v_add_f32_dpp v116, v116, v116 row_half_mirror row_mask:0xf bank_mask:0xf bound_ctrl:1
	v_cvt_pk_bf16_f32 v110, v110, v111
	v_cvt_pk_bf16_f32 v111, v152, v153
	v_add_f32_dpp v116, v116, v116 row_mirror row_mask:0xf bank_mask:0xf bound_ctrl:1
	global_store_dwordx2 v[158:159], v[108:109], off offset:1024
	global_store_dwordx2 v[158:159], v[110:111], off offset:3072
	v_readlane_b32 s4, v116, 16
	v_readlane_b32 s5, v116, 48
	v_readlane_b32 s0, v116, 0
	v_readlane_b32 s1, v116, 32
	v_mov_b32_e32 v116, s4
	v_mov_b32_e32 v117, s5
	v_pk_add_f32 v[116:117], s[0:1], v[116:117]
	v_cvt_pk_bf16_f32 v114, v156, v157
	v_add_f32_e32 v119, v116, v117
	v_add_f32_dpp v116, v118, v118 quad_perm:[1,0,3,2] row_mask:0xf bank_mask:0xf bound_ctrl:1
	v_fmamk_f32 v118, v119, 0x3a800000, v190
	v_rsq_f32_e32 v118, v118
	v_add_f32_dpp v116, v116, v116 quad_perm:[2,3,0,1] row_mask:0xf bank_mask:0xf bound_ctrl:1
	global_store_dwordx2 v[158:159], v[112:113], off offset:1536
	global_store_dwordx2 v[158:159], v[114:115], off offset:3584
	v_add_f32_dpp v116, v116, v116 row_half_mirror row_mask:0xf bank_mask:0xf bound_ctrl:1
	v_pk_mul_f32 v[86:87], v[86:87], v[118:119] op_sel_hi:[1,0]
	v_pk_mul_f32 v[82:83], v[82:83], v[118:119] op_sel_hi:[1,0]
	v_add_f32_dpp v116, v116, v116 row_mirror row_mask:0xf bank_mask:0xf bound_ctrl:1
	v_pk_mul_f32 v[74:75], v[74:75], v[118:119] op_sel_hi:[1,0]
	v_readlane_b32 s4, v116, 16
	v_readlane_b32 s5, v116, 48
	v_readlane_b32 s0, v116, 0
	v_readlane_b32 s1, v116, 32
	v_mov_b32_e32 v116, s4
	v_mov_b32_e32 v117, s5
	v_pk_add_f32 v[116:117], s[0:1], v[116:117]
	v_pk_mul_f32 v[70:71], v[70:71], v[118:119] op_sel_hi:[1,0]
	v_add_f32_e32 v116, v116, v117
	v_fmamk_f32 v116, v116, 0x3a800000, v190
	v_rsq_f32_e32 v116, v116
	v_pk_mul_f32 v[66:67], v[66:67], v[118:119] op_sel_hi:[1,0]
	v_pk_mul_f32 v[64:65], v[64:65], v[118:119] op_sel_hi:[1,0]
	v_pk_mul_f32 v[58:59], v[58:59], v[118:119] op_sel_hi:[1,0]
	v_pk_mul_f32 v[56:57], v[56:57], v[118:119] op_sel_hi:[1,0]
	v_readlane_b32 s0, v238, 18
	v_pk_fma_f32 v[82:83], v[82:83], v[4:5], v[12:13]
	v_pk_fma_f32 v[86:87], v[86:87], v[2:3], v[10:11]
	v_pk_mul_f32 v[84:85], v[84:85], v[116:117] op_sel_hi:[1,0]
	v_pk_mul_f32 v[80:81], v[80:81], v[116:117] op_sel_hi:[1,0]
	v_pk_fma_f32 v[70:71], v[70:71], v[8:9], v[16:17]
	v_pk_fma_f32 v[74:75], v[74:75], v[6:7], v[14:15]
	v_pk_mul_f32 v[72:73], v[72:73], v[116:117] op_sel_hi:[1,0]
	v_pk_mul_f32 v[68:69], v[68:69], v[116:117] op_sel_hi:[1,0]
	v_pk_fma_f32 v[64:65], v[64:65], v[20:21], v[28:29]
	v_pk_fma_f32 v[66:67], v[66:67], v[18:19], v[26:27]
	v_pk_mul_f32 v[62:63], v[62:63], v[116:117] op_sel_hi:[1,0]
	v_pk_mul_f32 v[60:61], v[60:61], v[116:117] op_sel_hi:[1,0]
	v_pk_fma_f32 v[56:57], v[56:57], v[24:25], v[32:33]
	v_pk_fma_f32 v[58:59], v[58:59], v[22:23], v[30:31]
	v_pk_mul_f32 v[54:55], v[54:55], v[116:117] op_sel_hi:[1,0]
	v_pk_mul_f32 v[52:53], v[52:53], v[116:117] op_sel_hi:[1,0]
	v_readlane_b32 s1, v238, 19
	v_pk_fma_f32 v[80:81], v[4:5], v[80:81], v[12:13]
	v_pk_fma_f32 v[84:85], v[2:3], v[84:85], v[10:11]
	v_pk_fma_f32 v[68:69], v[8:9], v[68:69], v[16:17]
	v_pk_fma_f32 v[72:73], v[6:7], v[72:73], v[14:15]
	v_pk_fma_f32 v[60:61], v[20:21], v[60:61], v[28:29]
	v_pk_fma_f32 v[62:63], v[18:19], v[62:63], v[26:27]
	v_pk_fma_f32 v[52:53], v[24:25], v[52:53], v[32:33]
	v_pk_fma_f32 v[54:55], v[22:23], v[54:55], v[30:31]
	v_lshl_add_u64 v[50:51], v[50:51], 0, s[0:1]
	v_cvt_pk_bf16_f32 v116, v86, v87
	v_cvt_pk_bf16_f32 v117, v82, v83
	v_cvt_pk_bf16_f32 v120, v74, v75
	v_cvt_pk_bf16_f32 v121, v70, v71
	v_cvt_pk_bf16_f32 v124, v66, v67
	v_cvt_pk_bf16_f32 v125, v64, v65
	v_cvt_pk_bf16_f32 v128, v58, v59
	v_cvt_pk_bf16_f32 v129, v56, v57
	v_cvt_pk_bf16_f32 v118, v84, v85
	v_cvt_pk_bf16_f32 v119, v80, v81
	global_store_dwordx2 v[50:51], v[116:117], off
	global_store_dwordx2 v[50:51], v[118:119], off offset:2048
	v_cvt_pk_bf16_f32 v122, v72, v73
	v_cvt_pk_bf16_f32 v123, v68, v69
	global_store_dwordx2 v[50:51], v[120:121], off offset:512
	global_store_dwordx2 v[50:51], v[122:123], off offset:2560
	v_cvt_pk_bf16_f32 v126, v62, v63
	v_cvt_pk_bf16_f32 v127, v60, v61
	global_store_dwordx2 v[50:51], v[124:125], off offset:1024
	global_store_dwordx2 v[50:51], v[126:127], off offset:3072
	v_cvt_pk_bf16_f32 v130, v54, v55
	v_cvt_pk_bf16_f32 v131, v52, v53
	global_store_dwordx2 v[50:51], v[128:129], off offset:1536
	global_store_dwordx2 v[50:51], v[130:131], off offset:3584
	global_load_dwordx4 v[50:53], v[38:39], off
	s_nop 0
	global_load_dwordx4 v[54:57], v[38:39], off offset:64
	global_load_dwordx4 v[58:61], v[38:39], off offset:128
	global_load_dwordx4 v[62:65], v[38:39], off offset:192
	global_load_dwordx4 v[66:69], v[38:39], off offset:256
	global_load_dwordx4 v[70:73], v[38:39], off offset:320
	v_readlane_b32 s0, v239, 31
	s_nop 1
	v_add_u32_e32 v74, s0, v47
	v_add_u32_e32 v80, 16, v74
	ds_write2st64_b64 v74, v[76:77], v[88:89] offset1:1
	ds_write2st64_b64 v80, v[78:79], v[90:91] offset0:4 offset1:5
	ds_write2st64_b64 v74, v[92:93], v[96:97] offset0:2 offset1:3
	global_load_dwordx4 v[74:77], v[38:39], off offset:384
	ds_write2st64_b64 v80, v[94:95], v[98:99] offset0:6 offset1:7
	v_readlane_b32 s0, v239, 47
	global_load_dwordx4 v[78:81], v[38:39], off offset:448
	s_nop 0
	v_add_u32_e32 v82, s0, v47
	v_add_u32_e32 v83, 16, v82
	ds_write2st64_b64 v82, v[132:133], v[136:137] offset1:1
	ds_write2st64_b64 v83, v[134:135], v[138:139] offset0:4 offset1:5
	ds_write2st64_b64 v82, v[140:141], v[144:145] offset0:2 offset1:3
	ds_write2st64_b64 v83, v[142:143], v[146:147] offset0:6 offset1:7
	global_load_dwordx4 v[82:85], v[38:39], off offset:512
	global_load_dwordx4 v[86:89], v[38:39], off offset:576
	v_readlane_b32 s0, v239, 46
	s_nop 1
	v_add_u32_e32 v90, s0, v47
	v_add_u32_e32 v91, 16, v90
	ds_write2st64_b64 v90, v[100:101], v[104:105] offset1:1
	ds_write2st64_b64 v91, v[102:103], v[106:107] offset0:4 offset1:5
	ds_write2st64_b64 v90, v[108:109], v[112:113] offset0:2 offset1:3
	ds_write2st64_b64 v91, v[110:111], v[114:115] offset0:6 offset1:7
	global_load_dwordx4 v[90:93], v[38:39], off offset:640
	v_readlane_b32 s0, v239, 48
	s_nop 1
	v_add_u32_e32 v94, s0, v47
	v_add_u32_e32 v95, 16, v94
	ds_write2st64_b64 v94, v[116:117], v[120:121] offset1:1
	ds_write2st64_b64 v95, v[118:119], v[122:123] offset0:4 offset1:5
	ds_write2st64_b64 v94, v[124:125], v[128:129] offset0:2 offset1:3
	ds_write2st64_b64 v95, v[126:127], v[130:131] offset0:6 offset1:7
	global_load_dwordx4 v[94:97], v[38:39], off offset:704
	global_load_dwordx4 v[98:101], v[38:39], off offset:768
	global_load_dwordx4 v[102:105], v[38:39], off offset:832
	global_load_dwordx4 v[106:109], v[38:39], off offset:896
	global_load_dwordx4 v[110:113], v[38:39], off offset:960
	global_load_dwordx4 v[114:117], v[38:39], off offset:1024
	global_load_dwordx4 v[118:121], v[38:39], off offset:1088
	global_load_dwordx4 v[122:125], v[38:39], off offset:1152
	global_load_dwordx4 v[126:129], v[38:39], off offset:1216
	global_load_dwordx4 v[130:133], v[38:39], off offset:1280
	global_load_dwordx4 v[134:137], v[38:39], off offset:1344
	global_load_dwordx4 v[138:141], v[38:39], off offset:1408
	global_load_dwordx4 v[142:145], v[38:39], off offset:1472
	global_load_dwordx4 v[146:149], v[38:39], off offset:1536
	global_load_dwordx4 v[150:153], v[38:39], off offset:1600
	global_load_dwordx4 v[154:157], v[38:39], off offset:1664
	global_load_dwordx4 v[158:161], v[38:39], off offset:1728
	global_load_dwordx4 v[162:165], v[38:39], off offset:1792
	global_load_dwordx4 v[172:175], v[38:39], off offset:1856
	global_load_dwordx4 v[176:179], v[38:39], off offset:1920
	global_load_dwordx4 v[180:183], v[38:39], off offset:1984
	global_load_dwordx4 v[204:207], v[40:41], off
	s_waitcnt lgkmcnt(0)
	s_barrier
	ds_read_b128 v[208:211], v201
	ds_read_b128 v[212:215], v201 offset:64
	s_waitcnt vmcnt(32) lgkmcnt(1)
	v_mfma_f32_16x16x32_bf16 v[50:53], v[50:53], v[208:211], 0
	v_readlane_b32 s0, v239, 28
	v_readlane_b32 s1, v239, 29
	s_andn2_b64 vcc, exec, s[0:1]
	s_waitcnt vmcnt(31) lgkmcnt(0)
	v_mfma_f32_16x16x32_bf16 v[50:53], v[54:57], v[212:215], v[50:53]
	ds_read_b128 v[54:57], v201 offset:128
	ds_read_b128 v[208:211], v201 offset:192
	s_waitcnt vmcnt(30) lgkmcnt(1)
	v_mfma_f32_16x16x32_bf16 v[50:53], v[58:61], v[54:57], v[50:53]
	ds_read_b128 v[54:57], v201 offset:256
	ds_read_b128 v[58:61], v201 offset:320
	s_waitcnt vmcnt(29) lgkmcnt(2)
	v_mfma_f32_16x16x32_bf16 v[50:53], v[62:65], v[208:211], v[50:53]
	s_waitcnt vmcnt(28) lgkmcnt(1)
	v_mfma_f32_16x16x32_bf16 v[50:53], v[66:69], v[54:57], v[50:53]
	s_waitcnt vmcnt(27) lgkmcnt(0)
	v_mfma_f32_16x16x32_bf16 v[50:53], v[70:73], v[58:61], v[50:53]
	ds_read_b128 v[54:57], v201 offset:384
	ds_read_b128 v[58:61], v201 offset:448
	s_waitcnt vmcnt(26) lgkmcnt(1)
	v_mfma_f32_16x16x32_bf16 v[50:53], v[74:77], v[54:57], v[50:53]
	s_waitcnt vmcnt(25) lgkmcnt(0)
	v_mfma_f32_16x16x32_bf16 v[50:53], v[78:81], v[58:61], v[50:53]
	ds_read_b128 v[54:57], v201 offset:512
	ds_read_b128 v[58:61], v201 offset:576
	s_waitcnt vmcnt(24) lgkmcnt(1)
	v_mfma_f32_16x16x32_bf16 v[50:53], v[82:85], v[54:57], v[50:53]
	s_waitcnt vmcnt(23) lgkmcnt(0)
	v_mfma_f32_16x16x32_bf16 v[50:53], v[86:89], v[58:61], v[50:53]
	ds_read_b128 v[54:57], v201 offset:640
	ds_read_b128 v[58:61], v201 offset:704
	s_waitcnt vmcnt(22) lgkmcnt(1)
	v_mfma_f32_16x16x32_bf16 v[50:53], v[90:93], v[54:57], v[50:53]
	s_waitcnt vmcnt(21) lgkmcnt(0)
	v_mfma_f32_16x16x32_bf16 v[50:53], v[94:97], v[58:61], v[50:53]
	ds_read_b128 v[54:57], v201 offset:768
	ds_read_b128 v[58:61], v201 offset:832
	s_waitcnt vmcnt(20) lgkmcnt(1)
	v_mfma_f32_16x16x32_bf16 v[50:53], v[98:101], v[54:57], v[50:53]
	s_waitcnt vmcnt(19) lgkmcnt(0)
	v_mfma_f32_16x16x32_bf16 v[50:53], v[102:105], v[58:61], v[50:53]
	ds_read_b128 v[54:57], v201 offset:896
	ds_read_b128 v[58:61], v201 offset:960
	s_waitcnt vmcnt(18) lgkmcnt(1)
	v_mfma_f32_16x16x32_bf16 v[50:53], v[106:109], v[54:57], v[50:53]
	s_waitcnt vmcnt(17) lgkmcnt(0)
	v_mfma_f32_16x16x32_bf16 v[50:53], v[110:113], v[58:61], v[50:53]
	ds_read_b128 v[54:57], v201 offset:1024
	ds_read_b128 v[58:61], v201 offset:1088
	s_waitcnt vmcnt(16) lgkmcnt(1)
	v_mfma_f32_16x16x32_bf16 v[50:53], v[114:117], v[54:57], v[50:53]
	s_waitcnt vmcnt(15) lgkmcnt(0)
	v_mfma_f32_16x16x32_bf16 v[50:53], v[118:121], v[58:61], v[50:53]
	ds_read_b128 v[54:57], v201 offset:1152
	ds_read_b128 v[58:61], v201 offset:1216
	s_waitcnt vmcnt(14) lgkmcnt(1)
	v_mfma_f32_16x16x32_bf16 v[50:53], v[122:125], v[54:57], v[50:53]
	s_waitcnt vmcnt(13) lgkmcnt(0)
	v_mfma_f32_16x16x32_bf16 v[50:53], v[126:129], v[58:61], v[50:53]
	ds_read_b128 v[54:57], v201 offset:1280
	ds_read_b128 v[58:61], v201 offset:1344
	s_waitcnt vmcnt(12) lgkmcnt(1)
	v_mfma_f32_16x16x32_bf16 v[50:53], v[130:133], v[54:57], v[50:53]
	s_waitcnt vmcnt(11) lgkmcnt(0)
	v_mfma_f32_16x16x32_bf16 v[50:53], v[134:137], v[58:61], v[50:53]
	ds_read_b128 v[54:57], v201 offset:1408
	ds_read_b128 v[58:61], v201 offset:1472
	s_waitcnt vmcnt(10) lgkmcnt(1)
	v_mfma_f32_16x16x32_bf16 v[50:53], v[138:141], v[54:57], v[50:53]
	s_waitcnt vmcnt(9) lgkmcnt(0)
	v_mfma_f32_16x16x32_bf16 v[50:53], v[142:145], v[58:61], v[50:53]
	ds_read_b128 v[54:57], v201 offset:1536
	ds_read_b128 v[58:61], v201 offset:1600
	s_waitcnt vmcnt(8) lgkmcnt(1)
	v_mfma_f32_16x16x32_bf16 v[50:53], v[146:149], v[54:57], v[50:53]
	s_waitcnt vmcnt(7) lgkmcnt(0)
	v_mfma_f32_16x16x32_bf16 v[50:53], v[150:153], v[58:61], v[50:53]
	ds_read_b128 v[54:57], v201 offset:1664
	ds_read_b128 v[58:61], v201 offset:1728
	s_waitcnt vmcnt(6) lgkmcnt(1)
	v_mfma_f32_16x16x32_bf16 v[50:53], v[154:157], v[54:57], v[50:53]
	s_waitcnt vmcnt(5) lgkmcnt(0)
	v_mfma_f32_16x16x32_bf16 v[50:53], v[158:161], v[58:61], v[50:53]
	ds_read_b128 v[54:57], v201 offset:1792
	ds_read_b128 v[58:61], v201 offset:1856
	s_waitcnt vmcnt(4) lgkmcnt(1)
	v_mfma_f32_16x16x32_bf16 v[50:53], v[162:165], v[54:57], v[50:53]
	s_waitcnt vmcnt(3) lgkmcnt(0)
	v_mfma_f32_16x16x32_bf16 v[50:53], v[172:175], v[58:61], v[50:53]
	ds_read_b128 v[54:57], v201 offset:1920
	ds_read_b128 v[58:61], v201 offset:1984
	s_waitcnt vmcnt(2) lgkmcnt(1)
	v_mfma_f32_16x16x32_bf16 v[50:53], v[176:179], v[54:57], v[50:53]
	s_waitcnt vmcnt(1) lgkmcnt(0)
	v_mfma_f32_16x16x32_bf16 v[50:53], v[180:183], v[58:61], v[50:53]
	s_waitcnt vmcnt(0)
	s_nop 6
	v_pk_add_f32 v[50:51], v[50:51], v[204:205]
	v_pk_add_f32 v[52:53], v[52:53], v[206:207]
	ds_write2_b32 v166, v50, v51 offset1:1
	ds_write2_b32 v166, v52, v53 offset0:2 offset1:3
	s_waitcnt lgkmcnt(0)
	s_barrier
	s_cbranch_vccnz .LBB0_681
	ds_read2_b32 v[80:81], v202 offset1:1
	ds_read2_b32 v[78:79], v202 offset0:2 offset1:3
	ds_read2_b32 v[76:77], v202 offset0:4 offset1:5
	ds_read2_b32 v[74:75], v202 offset0:6 offset1:7
	ds_read2_b32 v[72:73], v202 offset0:8 offset1:9
	ds_read2_b32 v[70:71], v202 offset0:10 offset1:11
	ds_read2_b32 v[68:69], v202 offset0:12 offset1:13
	ds_read2_b32 v[66:67], v202 offset0:14 offset1:15
	ds_read2_b32 v[64:65], v202 offset0:16 offset1:17
	ds_read2_b32 v[62:63], v202 offset0:18 offset1:19
	ds_read2_b32 v[60:61], v202 offset0:20 offset1:21
	ds_read2_b32 v[58:59], v202 offset0:22 offset1:23
	ds_read2_b32 v[56:57], v202 offset0:24 offset1:25
	ds_read2_b32 v[54:55], v202 offset0:26 offset1:27
	ds_read2_b32 v[52:53], v202 offset0:28 offset1:29
	ds_read2_b32 v[50:51], v202 offset0:30 offset1:31
	s_waitcnt lgkmcnt(14)
	v_max_f32_e32 v82, v80, v80
	v_max_f32_e32 v82, 0xff61b1e6, v82
	v_cmp_gt_f32_e32 vcc, v81, v82
	s_mov_b32 s0, 0xff61b1e6
	v_cmp_lt_f32_e64 s[8:9], s0, v80
	v_cndmask_b32_e32 v82, v82, v81, vcc
	v_cndmask_b32_e64 v83, 0, 1, vcc
	v_cmp_gt_f32_e32 vcc, v78, v82
	s_nop 1
	v_cndmask_b32_e32 v82, v82, v78, vcc
	v_cndmask_b32_e64 v83, v83, 2, vcc
	v_cmp_gt_f32_e32 vcc, v79, v82
	s_nop 1
	v_cndmask_b32_e32 v82, v82, v79, vcc
	v_cndmask_b32_e64 v83, v83, 3, vcc
	s_waitcnt lgkmcnt(13)
	v_cmp_gt_f32_e32 vcc, v76, v82
	s_nop 1
	v_cndmask_b32_e32 v82, v82, v76, vcc
	v_cndmask_b32_e64 v83, v83, 4, vcc
	v_cmp_gt_f32_e32 vcc, v77, v82
	s_nop 1
	v_cndmask_b32_e32 v82, v82, v77, vcc
	v_cndmask_b32_e64 v83, v83, 5, vcc
	s_waitcnt lgkmcnt(12)
	v_cmp_gt_f32_e32 vcc, v74, v82
	s_nop 1
	v_cndmask_b32_e32 v82, v82, v74, vcc
	v_cndmask_b32_e64 v83, v83, 6, vcc
	v_cmp_gt_f32_e32 vcc, v75, v82
	s_nop 1
	v_cndmask_b32_e32 v82, v82, v75, vcc
	v_cndmask_b32_e64 v83, v83, 7, vcc
	s_waitcnt lgkmcnt(11)
	v_cmp_gt_f32_e32 vcc, v72, v82
	s_nop 1
	v_cndmask_b32_e32 v82, v82, v72, vcc
	v_cndmask_b32_e64 v83, v83, 8, vcc
	v_cmp_gt_f32_e32 vcc, v73, v82
	s_nop 1
	v_cndmask_b32_e32 v82, v82, v73, vcc
	v_cndmask_b32_e64 v83, v83, 9, vcc
	s_waitcnt lgkmcnt(10)
	v_cmp_gt_f32_e32 vcc, v70, v82
	s_nop 1
	v_cndmask_b32_e32 v82, v82, v70, vcc
	v_cndmask_b32_e64 v83, v83, 10, vcc
	v_cmp_gt_f32_e32 vcc, v71, v82
	s_nop 1
	v_cndmask_b32_e32 v82, v82, v71, vcc
	v_cndmask_b32_e64 v83, v83, 11, vcc
	s_waitcnt lgkmcnt(9)
	v_cmp_gt_f32_e32 vcc, v68, v82
	s_nop 1
	v_cndmask_b32_e32 v82, v82, v68, vcc
	v_cndmask_b32_e64 v83, v83, 12, vcc
	v_cmp_gt_f32_e32 vcc, v69, v82
	s_nop 1
	v_cndmask_b32_e32 v82, v82, v69, vcc
	v_cndmask_b32_e64 v83, v83, 13, vcc
	s_waitcnt lgkmcnt(8)
	v_cmp_gt_f32_e32 vcc, v66, v82
	s_nop 1
	v_cndmask_b32_e32 v82, v82, v66, vcc
	v_cndmask_b32_e64 v83, v83, 14, vcc
	v_cmp_gt_f32_e32 vcc, v67, v82
	s_nop 1
	v_cndmask_b32_e32 v82, v82, v67, vcc
	v_cndmask_b32_e64 v83, v83, 15, vcc
	s_waitcnt lgkmcnt(7)
	v_cmp_gt_f32_e32 vcc, v64, v82
	s_nop 1
	v_cndmask_b32_e32 v82, v82, v64, vcc
	v_cndmask_b32_e64 v83, v83, 16, vcc
	v_cmp_gt_f32_e32 vcc, v65, v82
	s_nop 1
	v_cndmask_b32_e32 v82, v82, v65, vcc
	v_cndmask_b32_e64 v83, v83, 17, vcc
	s_waitcnt lgkmcnt(6)
	v_cmp_gt_f32_e32 vcc, v62, v82
	s_nop 1
	v_cndmask_b32_e32 v82, v82, v62, vcc
	v_cndmask_b32_e64 v83, v83, 18, vcc
	v_cmp_gt_f32_e32 vcc, v63, v82
	s_nop 1
	v_cndmask_b32_e32 v82, v82, v63, vcc
	v_cndmask_b32_e64 v83, v83, 19, vcc
	s_waitcnt lgkmcnt(5)
	v_cmp_gt_f32_e32 vcc, v60, v82
	s_nop 1
	v_cndmask_b32_e32 v82, v82, v60, vcc
	v_cndmask_b32_e64 v83, v83, 20, vcc
	v_cmp_gt_f32_e32 vcc, v61, v82
	s_nop 1
	v_cndmask_b32_e32 v82, v82, v61, vcc
	v_cndmask_b32_e64 v83, v83, 21, vcc
	s_waitcnt lgkmcnt(4)
	v_cmp_gt_f32_e32 vcc, v58, v82
	s_nop 1
	v_cndmask_b32_e32 v82, v82, v58, vcc
	v_cndmask_b32_e64 v83, v83, 22, vcc
	v_cmp_gt_f32_e32 vcc, v59, v82
	s_nop 1
	v_cndmask_b32_e32 v82, v82, v59, vcc
	v_cndmask_b32_e64 v83, v83, 23, vcc
	s_waitcnt lgkmcnt(3)
	v_cmp_gt_f32_e32 vcc, v56, v82
	s_nop 1
	v_cndmask_b32_e32 v82, v82, v56, vcc
	v_cndmask_b32_e64 v83, v83, 24, vcc
	v_cmp_gt_f32_e32 vcc, v57, v82
	s_nop 1
	v_cndmask_b32_e32 v82, v82, v57, vcc
	v_cndmask_b32_e64 v83, v83, 25, vcc
	s_waitcnt lgkmcnt(2)
	v_cmp_gt_f32_e32 vcc, v54, v82
	s_nop 1
	v_cndmask_b32_e32 v82, v82, v54, vcc
	v_cndmask_b32_e64 v83, v83, 26, vcc
	v_cmp_gt_f32_e32 vcc, v55, v82
	s_nop 1
	v_cndmask_b32_e32 v82, v82, v55, vcc
	v_cndmask_b32_e64 v83, v83, 27, vcc
	s_waitcnt lgkmcnt(1)
	v_cmp_gt_f32_e32 vcc, v52, v82
	s_nop 1
	v_cndmask_b32_e32 v82, v82, v52, vcc
	v_cndmask_b32_e64 v83, v83, 28, vcc
	v_cmp_gt_f32_e32 vcc, v53, v82
	s_nop 1
	v_cndmask_b32_e32 v82, v82, v53, vcc
	v_cndmask_b32_e64 v83, v83, 29, vcc
	s_waitcnt lgkmcnt(0)
	v_cmp_gt_f32_e32 vcc, v50, v82
	s_nop 1
	v_cndmask_b32_e32 v84, v82, v50, vcc
	v_cndmask_b32_e64 v82, v83, 30, vcc
	v_cmp_gt_f32_e32 vcc, v51, v84
	s_nop 1
	v_cndmask_b32_e64 v83, v82, 31, vcc
	v_cmp_ne_u32_e64 s[0:1], 0, v83
	s_and_b64 s[72:73], s[0:1], s[8:9]
	v_cndmask_b32_e64 v85, v197, v80, s[72:73]
	v_cmp_ne_u32_e64 s[68:69], 1, v83
	v_cmp_gt_f32_e64 s[0:1], v81, v85
	s_and_b64 s[0:1], s[68:69], s[0:1]
	v_cmp_ne_u32_e64 s[70:71], 2, v83
	v_cndmask_b32_e64 v85, v85, v81, s[0:1]
	v_cndmask_b32_e64 v86, 0, 1, s[0:1]
	v_cmp_gt_f32_e64 s[0:1], v78, v85
	s_and_b64 s[0:1], s[70:71], s[0:1]
	v_cmp_ne_u32_e64 s[66:67], 3, v83
	v_cndmask_b32_e64 v85, v85, v78, s[0:1]
	v_cndmask_b32_e64 v86, v86, 2, s[0:1]
	v_cmp_gt_f32_e64 s[0:1], v79, v85
	s_and_b64 s[0:1], s[66:67], s[0:1]
	v_cmp_ne_u32_e64 s[64:65], 4, v83
	v_cndmask_b32_e64 v85, v85, v79, s[0:1]
	v_cndmask_b32_e64 v86, v86, 3, s[0:1]
	v_cmp_gt_f32_e64 s[0:1], v76, v85
	s_and_b64 s[0:1], s[64:65], s[0:1]
	v_cmp_ne_u32_e64 s[62:63], 5, v83
	v_cndmask_b32_e64 v85, v85, v76, s[0:1]
	v_cndmask_b32_e64 v86, v86, 4, s[0:1]
	v_cmp_gt_f32_e64 s[0:1], v77, v85
	s_and_b64 s[0:1], s[62:63], s[0:1]
	v_cmp_ne_u32_e64 s[60:61], 6, v83
	v_cndmask_b32_e64 v85, v85, v77, s[0:1]
	v_cndmask_b32_e64 v86, v86, 5, s[0:1]
	v_cmp_gt_f32_e64 s[0:1], v74, v85
	s_and_b64 s[0:1], s[60:61], s[0:1]
	v_cmp_ne_u32_e64 s[58:59], 7, v83
	v_cndmask_b32_e64 v85, v85, v74, s[0:1]
	v_cndmask_b32_e64 v86, v86, 6, s[0:1]
	v_cmp_gt_f32_e64 s[0:1], v75, v85
	s_and_b64 s[0:1], s[58:59], s[0:1]
	v_cmp_ne_u32_e64 s[56:57], 8, v83
	v_cndmask_b32_e64 v85, v85, v75, s[0:1]
	v_cndmask_b32_e64 v86, v86, 7, s[0:1]
	v_cmp_gt_f32_e64 s[0:1], v72, v85
	s_and_b64 s[0:1], s[56:57], s[0:1]
	v_cmp_ne_u32_e64 s[54:55], 9, v83
	v_cndmask_b32_e64 v85, v85, v72, s[0:1]
	v_cndmask_b32_e64 v86, v86, 8, s[0:1]
	v_cmp_gt_f32_e64 s[0:1], v73, v85
	s_and_b64 s[0:1], s[54:55], s[0:1]
	v_cmp_ne_u32_e64 s[52:53], 10, v83
	v_cndmask_b32_e64 v85, v85, v73, s[0:1]
	v_cndmask_b32_e64 v86, v86, 9, s[0:1]
	v_cmp_gt_f32_e64 s[0:1], v70, v85
	s_and_b64 s[0:1], s[52:53], s[0:1]
	v_cmp_ne_u32_e64 s[50:51], 11, v83
	v_cndmask_b32_e64 v85, v85, v70, s[0:1]
	v_cndmask_b32_e64 v86, v86, 10, s[0:1]
	v_cmp_gt_f32_e64 s[0:1], v71, v85
	s_and_b64 s[0:1], s[50:51], s[0:1]
	v_cmp_ne_u32_e64 s[48:49], 12, v83
	v_cndmask_b32_e64 v85, v85, v71, s[0:1]
	v_cndmask_b32_e64 v86, v86, 11, s[0:1]
	v_cmp_gt_f32_e64 s[0:1], v68, v85
	s_and_b64 s[0:1], s[48:49], s[0:1]
	v_cmp_ne_u32_e64 s[46:47], 13, v83
	v_cndmask_b32_e64 v85, v85, v68, s[0:1]
	v_cndmask_b32_e64 v86, v86, 12, s[0:1]
	v_cmp_gt_f32_e64 s[0:1], v69, v85
	s_and_b64 s[0:1], s[46:47], s[0:1]
	v_cmp_ne_u32_e64 s[44:45], 14, v83
	v_cndmask_b32_e64 v85, v85, v69, s[0:1]
	v_cndmask_b32_e64 v86, v86, 13, s[0:1]
	v_cmp_gt_f32_e64 s[0:1], v66, v85
	s_and_b64 s[0:1], s[44:45], s[0:1]
	v_cmp_ne_u32_e64 s[42:43], 15, v83
	v_cndmask_b32_e64 v85, v85, v66, s[0:1]
	v_cndmask_b32_e64 v86, v86, 14, s[0:1]
	v_cmp_gt_f32_e64 s[0:1], v67, v85
	s_and_b64 s[0:1], s[42:43], s[0:1]
	v_cmp_ne_u32_e64 s[40:41], 16, v83
	v_cndmask_b32_e64 v85, v85, v67, s[0:1]
	v_cndmask_b32_e64 v86, v86, 15, s[0:1]
	v_cmp_gt_f32_e64 s[0:1], v64, v85
	s_and_b64 s[0:1], s[40:41], s[0:1]
	v_cmp_ne_u32_e64 s[38:39], 17, v83
	v_cndmask_b32_e64 v85, v85, v64, s[0:1]
	v_cndmask_b32_e64 v86, v86, 16, s[0:1]
	v_cmp_gt_f32_e64 s[0:1], v65, v85
	s_and_b64 s[0:1], s[38:39], s[0:1]
	v_cmp_ne_u32_e64 s[36:37], 18, v83
	v_cndmask_b32_e64 v85, v85, v65, s[0:1]
	v_cndmask_b32_e64 v86, v86, 17, s[0:1]
	v_cmp_gt_f32_e64 s[0:1], v62, v85
	s_and_b64 s[0:1], s[36:37], s[0:1]
	v_cmp_ne_u32_e64 s[34:35], 19, v83
	v_cndmask_b32_e64 v85, v85, v62, s[0:1]
	v_cndmask_b32_e64 v86, v86, 18, s[0:1]
	v_cmp_gt_f32_e64 s[0:1], v63, v85
	s_and_b64 s[0:1], s[34:35], s[0:1]
	v_cmp_ne_u32_e64 s[30:31], 20, v83
	v_cndmask_b32_e64 v85, v85, v63, s[0:1]
	v_cndmask_b32_e64 v86, v86, 19, s[0:1]
	v_cmp_gt_f32_e64 s[0:1], v60, v85
	s_and_b64 s[0:1], s[30:31], s[0:1]
	v_cmp_ne_u32_e64 s[28:29], 21, v83
	v_cndmask_b32_e64 v85, v85, v60, s[0:1]
	v_cndmask_b32_e64 v86, v86, 20, s[0:1]
	v_cmp_gt_f32_e64 s[0:1], v61, v85
	s_and_b64 s[0:1], s[28:29], s[0:1]
	v_cmp_ne_u32_e64 s[26:27], 22, v83
	v_cndmask_b32_e64 v85, v85, v61, s[0:1]
	v_cndmask_b32_e64 v86, v86, 21, s[0:1]
	v_cmp_gt_f32_e64 s[0:1], v58, v85
	s_and_b64 s[0:1], s[26:27], s[0:1]
	v_cmp_ne_u32_e64 s[24:25], 23, v83
	v_cndmask_b32_e64 v85, v85, v58, s[0:1]
	v_cndmask_b32_e64 v86, v86, 22, s[0:1]
	v_cmp_gt_f32_e64 s[0:1], v59, v85
	s_and_b64 s[0:1], s[24:25], s[0:1]
	v_cmp_ne_u32_e64 s[22:23], 24, v83
	v_cndmask_b32_e64 v85, v85, v59, s[0:1]
	v_cndmask_b32_e64 v86, v86, 23, s[0:1]
	v_cmp_gt_f32_e64 s[0:1], v56, v85
	s_and_b64 s[0:1], s[22:23], s[0:1]
	v_cmp_ne_u32_e64 s[20:21], 25, v83
	v_cndmask_b32_e64 v85, v85, v56, s[0:1]
	v_cndmask_b32_e64 v86, v86, 24, s[0:1]
	v_cmp_gt_f32_e64 s[0:1], v57, v85
	s_and_b64 s[0:1], s[20:21], s[0:1]
	v_cmp_ne_u32_e64 s[18:19], 26, v83
	v_cndmask_b32_e64 v85, v85, v57, s[0:1]
	v_cndmask_b32_e64 v86, v86, 25, s[0:1]
	v_cmp_gt_f32_e64 s[0:1], v54, v85
	s_and_b64 s[0:1], s[18:19], s[0:1]
	v_cmp_ne_u32_e64 s[16:17], 27, v83
	v_cndmask_b32_e64 v85, v85, v54, s[0:1]
	v_cndmask_b32_e64 v86, v86, 26, s[0:1]
	v_cmp_gt_f32_e64 s[0:1], v55, v85
	s_and_b64 s[0:1], s[16:17], s[0:1]
	v_cmp_ne_u32_e64 s[14:15], 28, v83
	v_cndmask_b32_e64 v85, v85, v55, s[0:1]
	v_cndmask_b32_e64 v86, v86, 27, s[0:1]
	v_cmp_gt_f32_e64 s[0:1], v52, v85
	s_and_b64 s[0:1], s[14:15], s[0:1]
	v_cmp_ne_u32_e64 s[12:13], 29, v83
	v_cndmask_b32_e64 v85, v85, v52, s[0:1]
	v_cndmask_b32_e64 v86, v86, 28, s[0:1]
	v_cmp_gt_f32_e64 s[0:1], v53, v85
	s_and_b64 s[0:1], s[12:13], s[0:1]
	v_cmp_ne_u32_e64 s[10:11], 30, v83
	v_cndmask_b32_e64 v85, v85, v53, s[0:1]
	v_cndmask_b32_e64 v87, v86, 29, s[0:1]
	v_cmp_gt_f32_e64 s[0:1], v50, v85
	s_and_b64 s[0:1], s[10:11], s[0:1]
	v_cmp_ne_u32_e64 s[6:7], 31, v83
	v_cndmask_b32_e64 v86, v85, v50, s[0:1]
	v_cndmask_b32_e64 v85, v87, 30, s[0:1]
	v_cmp_gt_f32_e64 s[0:1], v51, v86
	s_and_b64 s[4:5], s[6:7], s[0:1]
	v_cndmask_b32_e64 v85, v85, 31, s[4:5]
	v_cmp_ne_u32_e64 s[0:1], 0, v85
	s_and_b64 s[0:1], s[72:73], s[0:1]
	v_mov_b32_e32 v82, 0
	v_cndmask_b32_e64 v87, v197, v80, s[0:1]
	v_cmp_ne_u32_e64 s[0:1], 1, v85
	v_cmp_gt_f32_e64 s[72:73], v81, v87
	s_and_b64 s[68:69], s[68:69], s[0:1]
	s_and_b64 s[0:1], s[68:69], s[72:73]
	v_cndmask_b32_e64 v87, v87, v81, s[0:1]
	v_cndmask_b32_e64 v88, 0, 1, s[0:1]
	v_cmp_ne_u32_e64 s[0:1], 2, v85
	s_and_b64 s[70:71], s[70:71], s[0:1]
	v_cmp_gt_f32_e64 s[0:1], v78, v87
	s_and_b64 s[0:1], s[70:71], s[0:1]
	s_nop 0
	v_cndmask_b32_e64 v87, v87, v78, s[0:1]
	v_cndmask_b32_e64 v88, v88, 2, s[0:1]
	v_cmp_ne_u32_e64 s[0:1], 3, v85
	s_and_b64 s[66:67], s[66:67], s[0:1]
	v_cmp_gt_f32_e64 s[0:1], v79, v87
	s_and_b64 s[0:1], s[66:67], s[0:1]
	s_nop 0
	v_cndmask_b32_e64 v87, v87, v79, s[0:1]
	v_cndmask_b32_e64 v88, v88, 3, s[0:1]
	v_cmp_ne_u32_e64 s[0:1], 4, v85
	s_and_b64 s[64:65], s[64:65], s[0:1]
	v_cmp_gt_f32_e64 s[0:1], v76, v87
	s_and_b64 s[0:1], s[64:65], s[0:1]
	s_nop 0
	v_cndmask_b32_e64 v87, v87, v76, s[0:1]
	v_cndmask_b32_e64 v88, v88, 4, s[0:1]
	v_cmp_ne_u32_e64 s[0:1], 5, v85
	s_and_b64 s[62:63], s[62:63], s[0:1]
	v_cmp_gt_f32_e64 s[0:1], v77, v87
	s_and_b64 s[0:1], s[62:63], s[0:1]
	s_nop 0
	v_cndmask_b32_e64 v87, v87, v77, s[0:1]
	v_cndmask_b32_e64 v88, v88, 5, s[0:1]
	v_cmp_ne_u32_e64 s[0:1], 6, v85
	s_and_b64 s[60:61], s[60:61], s[0:1]
	v_cmp_gt_f32_e64 s[0:1], v74, v87
	s_and_b64 s[0:1], s[60:61], s[0:1]
	s_nop 0
	v_cndmask_b32_e64 v87, v87, v74, s[0:1]
	v_cndmask_b32_e64 v88, v88, 6, s[0:1]
	v_cmp_ne_u32_e64 s[0:1], 7, v85
	s_and_b64 s[58:59], s[58:59], s[0:1]
	v_cmp_gt_f32_e64 s[0:1], v75, v87
	s_and_b64 s[0:1], s[58:59], s[0:1]
	s_nop 0
	v_cndmask_b32_e64 v87, v87, v75, s[0:1]
	v_cndmask_b32_e64 v88, v88, 7, s[0:1]
	v_cmp_ne_u32_e64 s[0:1], 8, v85
	s_and_b64 s[56:57], s[56:57], s[0:1]
	v_cmp_gt_f32_e64 s[0:1], v72, v87
	s_and_b64 s[0:1], s[56:57], s[0:1]
	s_nop 0
	v_cndmask_b32_e64 v87, v87, v72, s[0:1]
	v_cndmask_b32_e64 v88, v88, 8, s[0:1]
	v_cmp_ne_u32_e64 s[0:1], 9, v85
	s_and_b64 s[54:55], s[54:55], s[0:1]
	v_cmp_gt_f32_e64 s[0:1], v73, v87
	s_and_b64 s[0:1], s[54:55], s[0:1]
	s_nop 0
	v_cndmask_b32_e64 v87, v87, v73, s[0:1]
	v_cndmask_b32_e64 v88, v88, 9, s[0:1]
	v_cmp_ne_u32_e64 s[0:1], 10, v85
	s_and_b64 s[52:53], s[52:53], s[0:1]
	v_cmp_gt_f32_e64 s[0:1], v70, v87
	s_and_b64 s[0:1], s[52:53], s[0:1]
	s_nop 0
	v_cndmask_b32_e64 v87, v87, v70, s[0:1]
	v_cndmask_b32_e64 v88, v88, 10, s[0:1]
	v_cmp_ne_u32_e64 s[0:1], 11, v85
	s_and_b64 s[50:51], s[50:51], s[0:1]
	v_cmp_gt_f32_e64 s[0:1], v71, v87
	s_and_b64 s[0:1], s[50:51], s[0:1]
	s_nop 0
	v_cndmask_b32_e64 v87, v87, v71, s[0:1]
	v_cndmask_b32_e64 v88, v88, 11, s[0:1]
	v_cmp_ne_u32_e64 s[0:1], 12, v85
	s_and_b64 s[48:49], s[48:49], s[0:1]
	v_cmp_gt_f32_e64 s[0:1], v68, v87
	s_and_b64 s[0:1], s[48:49], s[0:1]
	s_nop 0
	v_cndmask_b32_e64 v87, v87, v68, s[0:1]
	v_cndmask_b32_e64 v88, v88, 12, s[0:1]
	v_cmp_ne_u32_e64 s[0:1], 13, v85
	s_and_b64 s[46:47], s[46:47], s[0:1]
	v_cmp_gt_f32_e64 s[0:1], v69, v87
	s_and_b64 s[0:1], s[46:47], s[0:1]
	s_nop 0
	v_cndmask_b32_e64 v87, v87, v69, s[0:1]
	v_cndmask_b32_e64 v88, v88, 13, s[0:1]
	v_cmp_ne_u32_e64 s[0:1], 14, v85
	s_and_b64 s[44:45], s[44:45], s[0:1]
	v_cmp_gt_f32_e64 s[0:1], v66, v87
	s_and_b64 s[0:1], s[44:45], s[0:1]
	s_nop 0
	v_cndmask_b32_e64 v87, v87, v66, s[0:1]
	v_cndmask_b32_e64 v88, v88, 14, s[0:1]
	v_cmp_ne_u32_e64 s[0:1], 15, v85
	s_and_b64 s[42:43], s[42:43], s[0:1]
	v_cmp_gt_f32_e64 s[0:1], v67, v87
	s_and_b64 s[0:1], s[42:43], s[0:1]
	s_nop 0
	v_cndmask_b32_e64 v87, v87, v67, s[0:1]
	v_cndmask_b32_e64 v88, v88, 15, s[0:1]
	v_cmp_ne_u32_e64 s[0:1], 16, v85
	s_and_b64 s[40:41], s[40:41], s[0:1]
	v_cmp_gt_f32_e64 s[0:1], v64, v87
	s_and_b64 s[0:1], s[40:41], s[0:1]
	s_nop 0
	v_cndmask_b32_e64 v87, v87, v64, s[0:1]
	v_cndmask_b32_e64 v88, v88, 16, s[0:1]
	v_cmp_ne_u32_e64 s[0:1], 17, v85
	s_and_b64 s[38:39], s[38:39], s[0:1]
	v_cmp_gt_f32_e64 s[0:1], v65, v87
	s_and_b64 s[0:1], s[38:39], s[0:1]
	s_nop 0
	v_cndmask_b32_e64 v87, v87, v65, s[0:1]
	v_cndmask_b32_e64 v88, v88, 17, s[0:1]
	v_cmp_ne_u32_e64 s[0:1], 18, v85
	s_and_b64 s[36:37], s[36:37], s[0:1]
	v_cmp_gt_f32_e64 s[0:1], v62, v87
	s_and_b64 s[0:1], s[36:37], s[0:1]
	s_nop 0
	v_cndmask_b32_e64 v87, v87, v62, s[0:1]
	v_cndmask_b32_e64 v88, v88, 18, s[0:1]
	v_cmp_ne_u32_e64 s[0:1], 19, v85
	s_and_b64 s[34:35], s[34:35], s[0:1]
	v_cmp_gt_f32_e64 s[0:1], v63, v87
	s_and_b64 s[0:1], s[34:35], s[0:1]
	s_nop 0
	v_cndmask_b32_e64 v87, v87, v63, s[0:1]
	v_cndmask_b32_e64 v88, v88, 19, s[0:1]
	v_cmp_ne_u32_e64 s[0:1], 20, v85
	s_and_b64 s[30:31], s[30:31], s[0:1]
	v_cmp_gt_f32_e64 s[0:1], v60, v87
	s_and_b64 s[0:1], s[30:31], s[0:1]
	s_nop 0
	v_cndmask_b32_e64 v87, v87, v60, s[0:1]
	v_cndmask_b32_e64 v88, v88, 20, s[0:1]
	v_cmp_ne_u32_e64 s[0:1], 21, v85
	s_and_b64 s[28:29], s[28:29], s[0:1]
	v_cmp_gt_f32_e64 s[0:1], v61, v87
	s_and_b64 s[0:1], s[28:29], s[0:1]
	s_nop 0
	v_cndmask_b32_e64 v87, v87, v61, s[0:1]
	v_cndmask_b32_e64 v88, v88, 21, s[0:1]
	v_cmp_ne_u32_e64 s[0:1], 22, v85
	s_and_b64 s[26:27], s[26:27], s[0:1]
	v_cmp_gt_f32_e64 s[0:1], v58, v87
	s_and_b64 s[0:1], s[26:27], s[0:1]
	s_nop 0
	v_cndmask_b32_e64 v87, v87, v58, s[0:1]
	v_cndmask_b32_e64 v88, v88, 22, s[0:1]
	v_cmp_ne_u32_e64 s[0:1], 23, v85
	s_and_b64 s[24:25], s[24:25], s[0:1]
	v_cmp_gt_f32_e64 s[0:1], v59, v87
	s_and_b64 s[0:1], s[24:25], s[0:1]
	s_nop 0
	v_cndmask_b32_e64 v87, v87, v59, s[0:1]
	v_cndmask_b32_e64 v88, v88, 23, s[0:1]
	v_cmp_ne_u32_e64 s[0:1], 24, v85
	s_and_b64 s[22:23], s[22:23], s[0:1]
	v_cmp_gt_f32_e64 s[0:1], v56, v87
	s_and_b64 s[0:1], s[22:23], s[0:1]
	s_nop 0
	v_cndmask_b32_e64 v87, v87, v56, s[0:1]
	v_cndmask_b32_e64 v88, v88, 24, s[0:1]
	v_cmp_ne_u32_e64 s[0:1], 25, v85
	s_and_b64 s[20:21], s[20:21], s[0:1]
	v_cmp_gt_f32_e64 s[0:1], v57, v87
	s_and_b64 s[0:1], s[20:21], s[0:1]
	s_nop 0
	v_cndmask_b32_e64 v87, v87, v57, s[0:1]
	v_cndmask_b32_e64 v88, v88, 25, s[0:1]
	v_cmp_ne_u32_e64 s[0:1], 26, v85
	s_and_b64 s[18:19], s[18:19], s[0:1]
	v_cmp_gt_f32_e64 s[0:1], v54, v87
	s_and_b64 s[0:1], s[18:19], s[0:1]
	s_nop 0
	v_cndmask_b32_e64 v87, v87, v54, s[0:1]
	v_cndmask_b32_e64 v88, v88, 26, s[0:1]
	v_cmp_ne_u32_e64 s[0:1], 27, v85
	s_and_b64 s[16:17], s[16:17], s[0:1]
	v_cmp_gt_f32_e64 s[0:1], v55, v87
	s_and_b64 s[0:1], s[16:17], s[0:1]
	s_nop 0
	v_cndmask_b32_e64 v87, v87, v55, s[0:1]
	v_cndmask_b32_e64 v88, v88, 27, s[0:1]
	v_cmp_ne_u32_e64 s[0:1], 28, v85
	s_and_b64 s[14:15], s[14:15], s[0:1]
	v_cmp_gt_f32_e64 s[0:1], v52, v87
	s_and_b64 s[0:1], s[14:15], s[0:1]
	s_nop 0
	v_cndmask_b32_e64 v87, v87, v52, s[0:1]
	v_cndmask_b32_e64 v88, v88, 28, s[0:1]
	v_cmp_ne_u32_e64 s[0:1], 29, v85
	s_and_b64 s[12:13], s[12:13], s[0:1]
	v_cmp_gt_f32_e64 s[0:1], v53, v87
	s_and_b64 s[0:1], s[12:13], s[0:1]
	s_nop 0
	v_cndmask_b32_e64 v87, v87, v53, s[0:1]
	v_cndmask_b32_e64 v89, v88, 29, s[0:1]
	v_cmp_ne_u32_e64 s[0:1], 30, v85
	s_and_b64 s[10:11], s[10:11], s[0:1]
	v_cmp_gt_f32_e64 s[0:1], v50, v87
	s_and_b64 s[0:1], s[10:11], s[0:1]
	v_cmp_eq_u32_e64 s[10:11], 0, v85
	v_cndmask_b32_e64 v88, v87, v50, s[0:1]
	v_cndmask_b32_e64 v87, v89, 30, s[0:1]
	v_cmp_ne_u32_e64 s[0:1], 31, v85
	s_and_b64 s[6:7], s[6:7], s[0:1]
	v_cmp_gt_f32_e64 s[0:1], v51, v88
	s_and_b64 s[6:7], s[6:7], s[0:1]
	v_cndmask_b32_e64 v87, v87, 31, s[6:7]
	v_cmp_ne_u32_e64 s[12:13], 0, v87
	v_cmp_eq_u32_e64 s[0:1], 0, v83
	s_and_b64 s[8:9], s[12:13], s[8:9]
	v_cndmask_b32_e64 v80, v197, v80, s[8:9]
	s_or_b64 s[0:1], s[0:1], s[10:11]
	v_cndmask_b32_e64 v80, v80, v197, s[0:1]
	s_and_saveexec_b64 s[10:11], s[68:69]
	v_cmp_ne_u32_e64 s[0:1], 1, v87
	v_cmp_gt_f32_e64 s[8:9], v81, v80
	s_and_b64 s[0:1], s[0:1], s[8:9]
	v_cndmask_b32_e64 v80, v80, v81, s[0:1]
	v_cndmask_b32_e64 v82, 0, 1, s[0:1]
	s_or_b64 exec, exec, s[10:11]
	v_cmp_ne_u32_e64 s[0:1], 2, v83
	v_cmp_ne_u32_e64 s[8:9], 2, v85
	s_and_b64 s[0:1], s[0:1], s[8:9]
	s_and_saveexec_b64 s[10:11], s[0:1]
	v_cmp_ne_u32_e64 s[0:1], 2, v87
	v_cmp_gt_f32_e64 s[8:9], v78, v80
	s_and_b64 s[0:1], s[0:1], s[8:9]
	v_cndmask_b32_e64 v80, v80, v78, s[0:1]
	v_cndmask_b32_e64 v82, v82, 2, s[0:1]
	s_or_b64 exec, exec, s[10:11]
	v_cmp_ne_u32_e64 s[0:1], 3, v83
	v_cmp_ne_u32_e64 s[8:9], 3, v85
	s_and_b64 s[0:1], s[0:1], s[8:9]
	s_and_saveexec_b64 s[10:11], s[0:1]
	v_readlane_b32 s70, v238, 32
	s_movk_i32 s69, 0x4000
	s_mov_b32 s67, 0x8000
	v_readlane_b32 s68, v238, 34
	v_readlane_b32 s71, v238, 33
	v_cmp_ne_u32_e64 s[0:1], 3, v87
	v_cmp_gt_f32_e64 s[8:9], v79, v80
	s_and_b64 s[0:1], s[0:1], s[8:9]
	v_cndmask_b32_e64 v80, v80, v79, s[0:1]
	v_cndmask_b32_e64 v82, v82, 3, s[0:1]
	s_or_b64 exec, exec, s[10:11]
	v_cmp_ne_u32_e64 s[0:1], 4, v83
	v_cmp_ne_u32_e64 s[8:9], 4, v85
	s_and_b64 s[0:1], s[0:1], s[8:9]
	s_and_saveexec_b64 s[10:11], s[0:1]
	v_cmp_ne_u32_e64 s[0:1], 4, v87
	v_cmp_gt_f32_e64 s[8:9], v76, v80
	s_and_b64 s[0:1], s[0:1], s[8:9]
	v_cndmask_b32_e64 v80, v80, v76, s[0:1]
	v_cndmask_b32_e64 v82, v82, 4, s[0:1]
	s_or_b64 exec, exec, s[10:11]
	v_cmp_ne_u32_e64 s[0:1], 5, v83
	v_cmp_ne_u32_e64 s[8:9], 5, v85
	s_and_b64 s[0:1], s[0:1], s[8:9]
	s_and_saveexec_b64 s[10:11], s[0:1]
	v_cmp_ne_u32_e64 s[0:1], 5, v87
	v_cmp_gt_f32_e64 s[8:9], v77, v80
	s_and_b64 s[0:1], s[0:1], s[8:9]
	v_cndmask_b32_e64 v80, v80, v77, s[0:1]
	v_cndmask_b32_e64 v82, v82, 5, s[0:1]
	s_or_b64 exec, exec, s[10:11]
	v_cmp_ne_u32_e64 s[0:1], 6, v83
	v_cmp_ne_u32_e64 s[8:9], 6, v85
	s_and_b64 s[0:1], s[0:1], s[8:9]
	s_and_saveexec_b64 s[10:11], s[0:1]
	v_cmp_ne_u32_e64 s[0:1], 6, v87
	v_cmp_gt_f32_e64 s[8:9], v74, v80
	s_and_b64 s[0:1], s[0:1], s[8:9]
	v_cndmask_b32_e64 v80, v80, v74, s[0:1]
	v_cndmask_b32_e64 v82, v82, 6, s[0:1]
	s_or_b64 exec, exec, s[10:11]
	v_cmp_ne_u32_e64 s[0:1], 7, v83
	v_cmp_ne_u32_e64 s[8:9], 7, v85
	s_and_b64 s[0:1], s[0:1], s[8:9]
	s_and_saveexec_b64 s[10:11], s[0:1]
	v_cmp_ne_u32_e64 s[0:1], 7, v87
	v_cmp_gt_f32_e64 s[8:9], v75, v80
	s_and_b64 s[0:1], s[0:1], s[8:9]
	v_cndmask_b32_e64 v80, v80, v75, s[0:1]
	v_cndmask_b32_e64 v82, v82, 7, s[0:1]
	s_or_b64 exec, exec, s[10:11]
	v_cmp_ne_u32_e64 s[0:1], 8, v83
	v_cmp_ne_u32_e64 s[8:9], 8, v85
	s_and_b64 s[0:1], s[0:1], s[8:9]
	s_and_saveexec_b64 s[10:11], s[0:1]
	v_cmp_ne_u32_e64 s[0:1], 8, v87
	v_cmp_gt_f32_e64 s[8:9], v72, v80
	s_and_b64 s[0:1], s[0:1], s[8:9]
	v_cndmask_b32_e64 v80, v80, v72, s[0:1]
	v_cndmask_b32_e64 v82, v82, 8, s[0:1]
	s_or_b64 exec, exec, s[10:11]
	v_cmp_ne_u32_e64 s[0:1], 9, v83
	v_cmp_ne_u32_e64 s[8:9], 9, v85
	s_and_b64 s[0:1], s[0:1], s[8:9]
	s_and_saveexec_b64 s[10:11], s[0:1]
	v_cmp_ne_u32_e64 s[0:1], 9, v87
	v_cmp_gt_f32_e64 s[8:9], v73, v80
	s_and_b64 s[0:1], s[0:1], s[8:9]
	v_cndmask_b32_e64 v80, v80, v73, s[0:1]
	v_cndmask_b32_e64 v82, v82, 9, s[0:1]
	s_or_b64 exec, exec, s[10:11]
	v_cmp_ne_u32_e64 s[0:1], 10, v83
	v_cmp_ne_u32_e64 s[8:9], 10, v85
	s_and_b64 s[0:1], s[0:1], s[8:9]
	s_and_saveexec_b64 s[10:11], s[0:1]
	v_cmp_ne_u32_e64 s[0:1], 10, v87
	v_cmp_gt_f32_e64 s[8:9], v70, v80
	s_and_b64 s[0:1], s[0:1], s[8:9]
	v_cndmask_b32_e64 v80, v80, v70, s[0:1]
	v_cndmask_b32_e64 v82, v82, 10, s[0:1]
	s_or_b64 exec, exec, s[10:11]
	v_cmp_ne_u32_e64 s[0:1], 11, v83
	v_cmp_ne_u32_e64 s[8:9], 11, v85
	s_and_b64 s[0:1], s[0:1], s[8:9]
	s_and_saveexec_b64 s[10:11], s[0:1]
	v_cmp_ne_u32_e64 s[0:1], 11, v87
	v_cmp_gt_f32_e64 s[8:9], v71, v80
	s_and_b64 s[0:1], s[0:1], s[8:9]
	v_cndmask_b32_e64 v80, v80, v71, s[0:1]
	v_cndmask_b32_e64 v82, v82, 11, s[0:1]
	s_or_b64 exec, exec, s[10:11]
	v_cmp_ne_u32_e64 s[0:1], 12, v83
	v_cmp_ne_u32_e64 s[8:9], 12, v85
	s_and_b64 s[0:1], s[0:1], s[8:9]
	s_and_saveexec_b64 s[10:11], s[0:1]
	v_cmp_ne_u32_e64 s[0:1], 12, v87
	v_cmp_gt_f32_e64 s[8:9], v68, v80
	s_and_b64 s[0:1], s[0:1], s[8:9]
	v_cndmask_b32_e64 v80, v80, v68, s[0:1]
	v_cndmask_b32_e64 v82, v82, 12, s[0:1]
	s_or_b64 exec, exec, s[10:11]
	v_cmp_ne_u32_e64 s[0:1], 13, v83
	v_cmp_ne_u32_e64 s[8:9], 13, v85
	s_and_b64 s[0:1], s[0:1], s[8:9]
	s_and_saveexec_b64 s[10:11], s[0:1]
	v_cmp_ne_u32_e64 s[0:1], 13, v87
	v_cmp_gt_f32_e64 s[8:9], v69, v80
	s_and_b64 s[0:1], s[0:1], s[8:9]
	v_cndmask_b32_e64 v80, v80, v69, s[0:1]
	v_cndmask_b32_e64 v82, v82, 13, s[0:1]
	s_or_b64 exec, exec, s[10:11]
	v_cmp_ne_u32_e64 s[0:1], 14, v83
	v_cmp_ne_u32_e64 s[8:9], 14, v85
	s_and_b64 s[0:1], s[0:1], s[8:9]
	s_and_saveexec_b64 s[10:11], s[0:1]
	v_cmp_ne_u32_e64 s[0:1], 14, v87
	v_cmp_gt_f32_e64 s[8:9], v66, v80
	s_and_b64 s[0:1], s[0:1], s[8:9]
	v_cndmask_b32_e64 v80, v80, v66, s[0:1]
	v_cndmask_b32_e64 v82, v82, 14, s[0:1]
	s_or_b64 exec, exec, s[10:11]
	v_cmp_ne_u32_e64 s[0:1], 15, v83
	v_cmp_ne_u32_e64 s[8:9], 15, v85
	s_and_b64 s[0:1], s[0:1], s[8:9]
	s_and_saveexec_b64 s[10:11], s[0:1]
	v_cmp_ne_u32_e64 s[0:1], 15, v87
	v_cmp_gt_f32_e64 s[8:9], v67, v80
	s_and_b64 s[0:1], s[0:1], s[8:9]
	v_cndmask_b32_e64 v80, v80, v67, s[0:1]
	v_cndmask_b32_e64 v82, v82, 15, s[0:1]
	s_or_b64 exec, exec, s[10:11]
	v_cmp_ne_u32_e64 s[0:1], 16, v83
	v_cmp_ne_u32_e64 s[8:9], 16, v85
	s_and_b64 s[0:1], s[0:1], s[8:9]
	s_and_saveexec_b64 s[10:11], s[0:1]
	v_cmp_ne_u32_e64 s[0:1], 16, v87
	v_cmp_gt_f32_e64 s[8:9], v64, v80
	s_and_b64 s[0:1], s[0:1], s[8:9]
	v_cndmask_b32_e64 v80, v80, v64, s[0:1]
	v_cndmask_b32_e64 v82, v82, 16, s[0:1]
	s_or_b64 exec, exec, s[10:11]
	v_cmp_ne_u32_e64 s[0:1], 17, v83
	v_cmp_ne_u32_e64 s[8:9], 17, v85
	s_and_b64 s[0:1], s[0:1], s[8:9]
	s_and_saveexec_b64 s[10:11], s[0:1]
	v_cmp_ne_u32_e64 s[0:1], 17, v87
	v_cmp_gt_f32_e64 s[8:9], v65, v80
	s_and_b64 s[0:1], s[0:1], s[8:9]
	v_cndmask_b32_e64 v80, v80, v65, s[0:1]
	v_cndmask_b32_e64 v82, v82, 17, s[0:1]
	s_or_b64 exec, exec, s[10:11]
	v_cmp_ne_u32_e64 s[0:1], 18, v83
	v_cmp_ne_u32_e64 s[8:9], 18, v85
	s_and_b64 s[0:1], s[0:1], s[8:9]
	s_and_saveexec_b64 s[10:11], s[0:1]
	v_cmp_ne_u32_e64 s[0:1], 18, v87
	v_cmp_gt_f32_e64 s[8:9], v62, v80
	s_and_b64 s[0:1], s[0:1], s[8:9]
	v_cndmask_b32_e64 v80, v80, v62, s[0:1]
	v_cndmask_b32_e64 v82, v82, 18, s[0:1]
	s_or_b64 exec, exec, s[10:11]
	v_cmp_ne_u32_e64 s[0:1], 19, v83
	v_cmp_ne_u32_e64 s[8:9], 19, v85
	s_and_b64 s[0:1], s[0:1], s[8:9]
	s_and_saveexec_b64 s[10:11], s[0:1]
	v_cmp_ne_u32_e64 s[0:1], 19, v87
	v_cmp_gt_f32_e64 s[8:9], v63, v80
	s_and_b64 s[0:1], s[0:1], s[8:9]
	v_cndmask_b32_e64 v80, v80, v63, s[0:1]
	v_cndmask_b32_e64 v82, v82, 19, s[0:1]
	s_or_b64 exec, exec, s[10:11]
	v_cmp_ne_u32_e64 s[0:1], 20, v83
	v_cmp_ne_u32_e64 s[8:9], 20, v85
	s_and_b64 s[0:1], s[0:1], s[8:9]
	s_and_saveexec_b64 s[10:11], s[0:1]
	v_cmp_ne_u32_e64 s[0:1], 20, v87
	v_cmp_gt_f32_e64 s[8:9], v60, v80
	s_and_b64 s[0:1], s[0:1], s[8:9]
	v_cndmask_b32_e64 v80, v80, v60, s[0:1]
	v_cndmask_b32_e64 v82, v82, 20, s[0:1]
	s_or_b64 exec, exec, s[10:11]
	v_cmp_ne_u32_e64 s[0:1], 21, v83
	v_cmp_ne_u32_e64 s[8:9], 21, v85
	s_and_b64 s[0:1], s[0:1], s[8:9]
	s_and_saveexec_b64 s[10:11], s[0:1]
	v_cmp_ne_u32_e64 s[0:1], 21, v87
	v_cmp_gt_f32_e64 s[8:9], v61, v80
	s_and_b64 s[0:1], s[0:1], s[8:9]
	v_cndmask_b32_e64 v80, v80, v61, s[0:1]
	v_cndmask_b32_e64 v82, v82, 21, s[0:1]
	s_or_b64 exec, exec, s[10:11]
	v_cmp_ne_u32_e64 s[0:1], 22, v83
	v_cmp_ne_u32_e64 s[8:9], 22, v85
	s_and_b64 s[0:1], s[0:1], s[8:9]
	s_and_saveexec_b64 s[10:11], s[0:1]
	v_cmp_ne_u32_e64 s[0:1], 22, v87
	v_cmp_gt_f32_e64 s[8:9], v58, v80
	s_and_b64 s[0:1], s[0:1], s[8:9]
	v_cndmask_b32_e64 v80, v80, v58, s[0:1]
	v_cndmask_b32_e64 v82, v82, 22, s[0:1]
	s_or_b64 exec, exec, s[10:11]
	v_cmp_ne_u32_e64 s[0:1], 23, v83
	v_cmp_ne_u32_e64 s[8:9], 23, v85
	s_and_b64 s[0:1], s[0:1], s[8:9]
	s_and_saveexec_b64 s[10:11], s[0:1]
	v_cmp_ne_u32_e64 s[0:1], 23, v87
	v_cmp_gt_f32_e64 s[8:9], v59, v80
	s_and_b64 s[0:1], s[0:1], s[8:9]
	v_cndmask_b32_e64 v80, v80, v59, s[0:1]
	v_cndmask_b32_e64 v82, v82, 23, s[0:1]
	s_or_b64 exec, exec, s[10:11]
	v_cmp_ne_u32_e64 s[0:1], 24, v83
	v_cmp_ne_u32_e64 s[8:9], 24, v85
	s_and_b64 s[0:1], s[0:1], s[8:9]
	s_and_saveexec_b64 s[10:11], s[0:1]
	v_cmp_ne_u32_e64 s[0:1], 24, v87
	v_cmp_gt_f32_e64 s[8:9], v56, v80
	s_and_b64 s[0:1], s[0:1], s[8:9]
	v_cndmask_b32_e64 v80, v80, v56, s[0:1]
	v_cndmask_b32_e64 v82, v82, 24, s[0:1]
	s_or_b64 exec, exec, s[10:11]
	v_cmp_ne_u32_e64 s[0:1], 25, v83
	v_cmp_ne_u32_e64 s[8:9], 25, v85
	s_and_b64 s[0:1], s[0:1], s[8:9]
	s_and_saveexec_b64 s[10:11], s[0:1]
	v_cmp_ne_u32_e64 s[0:1], 25, v87
	v_cmp_gt_f32_e64 s[8:9], v57, v80
	s_and_b64 s[0:1], s[0:1], s[8:9]
	v_cndmask_b32_e64 v80, v80, v57, s[0:1]
	v_cndmask_b32_e64 v82, v82, 25, s[0:1]
	s_or_b64 exec, exec, s[10:11]
	v_cmp_ne_u32_e64 s[0:1], 26, v83
	v_cmp_ne_u32_e64 s[8:9], 26, v85
	s_and_b64 s[0:1], s[0:1], s[8:9]
	s_and_saveexec_b64 s[10:11], s[0:1]
	v_cmp_ne_u32_e64 s[0:1], 26, v87
	v_cmp_gt_f32_e64 s[8:9], v54, v80
	s_and_b64 s[0:1], s[0:1], s[8:9]
	v_cndmask_b32_e64 v80, v80, v54, s[0:1]
	v_cndmask_b32_e64 v82, v82, 26, s[0:1]
	s_or_b64 exec, exec, s[10:11]
	v_cmp_ne_u32_e64 s[0:1], 27, v83
	v_cmp_ne_u32_e64 s[8:9], 27, v85
	s_and_b64 s[0:1], s[0:1], s[8:9]
	s_and_saveexec_b64 s[10:11], s[0:1]
	v_cmp_ne_u32_e64 s[0:1], 27, v87
	v_cmp_gt_f32_e64 s[8:9], v55, v80
	s_and_b64 s[0:1], s[0:1], s[8:9]
	v_cndmask_b32_e64 v80, v80, v55, s[0:1]
	v_cndmask_b32_e64 v82, v82, 27, s[0:1]
	s_or_b64 exec, exec, s[10:11]
	v_cmp_ne_u32_e64 s[0:1], 28, v83
	v_cmp_ne_u32_e64 s[8:9], 28, v85
	s_and_b64 s[0:1], s[0:1], s[8:9]
	s_and_saveexec_b64 s[10:11], s[0:1]
	v_cmp_ne_u32_e64 s[0:1], 28, v87
	v_cmp_gt_f32_e64 s[8:9], v52, v80
	s_and_b64 s[0:1], s[0:1], s[8:9]
	v_cndmask_b32_e64 v80, v80, v52, s[0:1]
	v_cndmask_b32_e64 v82, v82, 28, s[0:1]
	s_or_b64 exec, exec, s[10:11]
	v_cmp_ne_u32_e64 s[0:1], 29, v83
	v_cmp_ne_u32_e64 s[8:9], 29, v85
	s_and_b64 s[0:1], s[0:1], s[8:9]
	s_and_saveexec_b64 s[10:11], s[0:1]
	v_cmp_ne_u32_e64 s[0:1], 29, v87
	v_cmp_gt_f32_e64 s[8:9], v53, v80
	s_and_b64 s[0:1], s[0:1], s[8:9]
	v_cndmask_b32_e64 v80, v80, v53, s[0:1]
	v_cndmask_b32_e64 v82, v82, 29, s[0:1]
	s_or_b64 exec, exec, s[10:11]
	v_cmp_ne_u32_e64 s[0:1], 30, v83
	v_cmp_ne_u32_e64 s[8:9], 30, v85
	s_and_b64 s[0:1], s[0:1], s[8:9]
	s_and_saveexec_b64 s[10:11], s[0:1]
	v_cmp_ne_u32_e64 s[0:1], 30, v87
	v_cmp_gt_f32_e64 s[8:9], v50, v80
	s_and_b64 s[0:1], s[0:1], s[8:9]
	v_cndmask_b32_e64 v80, v80, v50, s[0:1]
	v_cndmask_b32_e64 v82, v82, 30, s[0:1]
	s_or_b64 exec, exec, s[10:11]
	v_cmp_ne_u32_e64 s[0:1], 31, v83
	v_cmp_ne_u32_e64 s[8:9], 31, v85
	s_and_b64 s[0:1], s[0:1], s[8:9]
	s_and_saveexec_b64 s[10:11], s[0:1]
	v_cmp_ne_u32_e64 s[0:1], 31, v87
	v_cmp_gt_f32_e64 s[8:9], v51, v80
	s_and_b64 s[0:1], s[0:1], s[8:9]
	v_cndmask_b32_e64 v80, v80, v51, s[0:1]
	v_cndmask_b32_e64 v82, v82, 31, s[0:1]
	s_or_b64 exec, exec, s[10:11]
	v_mov_b32_e32 v54, 0
	s_mov_b32 s16, 0
	v_mov_b32_e32 v53, 0
	v_mov_b32_e32 v52, 0
	v_mov_b32_e32 v50, 0
	v_mov_b32_e32 v55, 0
